# speedup vs baseline: 1.0960x; 1.0063x over previous
_Z7k_layerILi1EEvPKDF16_S1_PKfS3_S3_S3_S3_S3_S1_S1_S1_S1_S3_S3_PKhS5_PDF16_S6_PfS7_:
	s_ashr_i32 s3, s2, 1
	s_and_b32 s3, s3, -8
	s_and_b32 s16, s2, 7
	v_readfirstlane_b32 s15, v0
	s_or_b32 s12, s3, s16
	s_bfe_u32 s14, s2, 0x10003
	s_cmpk_gt_u32 s15, 0xff
	s_mov_b64 s[2:3], -1
	s_cbranch_scc0 .LBB2_17
	s_mov_b32 s72, 0x2000
	s_mov_b32 s73, 0x4000
	s_mov_b32 s74, 0x6000
	s_mov_b32 s75, 0x8000
	s_mov_b32 s76, 0xa000
	s_mov_b32 s77, 0xc000
	s_mov_b32 s78, 0xe000
	s_lshl_b32 s70, s12, 17
	s_lshl_b32 s66, s14, 7
	s_or_b32 s70, s70, s66
	s_mov_b32 s66, 0x18000
	s_mov_b32 s67, 0x1a000
	s_mov_b32 s68, 0x1c000
	s_mov_b32 s69, 0x1e000
	v_add_u32_e32 v165, 0xffffff00, v0
	v_lshrrev_b32_e32 v163, 3, v165
	v_and_b32_e32 v165, 7, v165
	v_lshlrev_b32_e32 v165, 4, v165
	v_mul_u32_u24_e32 v162, 0x90, v163
	v_add_u32_e32 v162, v162, v165
	v_add_u32_e32 v162, 0x11000, v162
	v_lshl_add_u32 v163, v163, 8, v165
	v_add_u32_e32 v163, s70, v163
	s_mov_b32 s44, 0x3e000000
	v_mov_b32_e32 v240, 0x64646464
	s_mov_b32 s42, 0x4010400
	s_mov_b32 s43, 0x4030402
	s_load_dwordx2 s[4:5], s[0:1], 0x80
	s_load_dwordx2 s[8:9], s[0:1], 0x0
	v_lshlrev_b32_e32 v2, 3, v0
	v_add_u32_e32 v1, 0xffffff00, v0
	v_ashrrev_i32_e32 v3, 4, v1
	v_and_b32_e32 v38, 0x78, v2
	s_lshl_b32 s17, s12, 9
	v_add_u32_e32 v2, s17, v3
	v_lshlrev_b32_e32 v4, 1, v38
	s_mov_b32 s7, 0x20000
	s_mov_b32 s6, 0x1000000
	v_lshl_or_b32 v2, v2, 8, v4
	s_waitcnt lgkmcnt(0)
	s_and_b32 s9, s9, 0xffff
	s_mov_b32 s10, s6
	s_mov_b32 s11, s7
	v_add_u32_e32 v5, 0x4000, v2
	buffer_load_dwordx4 v[10:13], v2, s[8:11], 0 offen sc1
	buffer_load_dwordx4 v[18:21], v5, s[8:11], 0 offen sc1
	v_add_u32_e32 v5, 0x1000, v2
	buffer_load_dwordx4 v[26:29], v5, s[8:11], 0 offen sc1
	v_add_u32_e32 v5, 0x2000, v2
	v_add_u32_e32 v6, 0x3000, v2
	buffer_load_dwordx4 v[30:33], v5, s[8:11], 0 offen sc1
	buffer_load_dwordx4 v[58:61], v6, s[8:11], 0 offen sc1
	v_add_u32_e32 v5, 0x5000, v2
	buffer_load_dwordx4 v[34:37], v5, s[8:11], 0 offen sc1
	v_add_u32_e32 v5, 0x6000, v2
	v_add_u32_e32 v2, 0x7000, v2
	buffer_load_dwordx4 v[62:65], v5, s[8:11], 0 offen sc1
	buffer_load_dwordx4 v[66:69], v2, s[8:11], 0 offen sc1
	s_or_b32 s2, s17, 0x80
	v_add_u32_e32 v2, s2, v3
	v_lshl_or_b32 v6, v2, 8, v4
	v_add_u32_e32 v2, 0x1000, v6
	v_add_u32_e32 v7, 0x2000, v6
	v_add_u32_e32 v8, 0x3000, v6
	buffer_load_dwordx4 v[70:73], v6, s[8:11], 0 offen sc1
	buffer_load_dwordx4 v[74:77], v2, s[8:11], 0 offen sc1
	buffer_load_dwordx4 v[14:17], v7, s[8:11], 0 offen sc1
	s_nop 0
	buffer_load_dwordx4 v[2:5], v8, s[8:11], 0 offen sc1
	v_add_u32_e32 v7, 0x4000, v6
	v_add_u32_e32 v8, 0x5000, v6
	v_add_u32_e32 v39, 0x6000, v6
	buffer_load_dwordx4 v[78:81], v7, s[8:11], 0 offen sc1
	buffer_load_dwordx4 v[82:85], v8, s[8:11], 0 offen sc1
	v_add_u32_e32 v40, 0x7000, v6
	buffer_load_dwordx4 v[22:25], v39, s[8:11], 0 offen sc1
	buffer_load_dwordx4 v[6:9], v40, s[8:11], 0 offen sc1
	v_lshlrev_b32_e32 v48, 2, v38
	v_or_b32_e32 v38, 0x1e600, v48
	s_barrier
	ds_read_b128 v[38:41], v38
	v_or_b32_e32 v42, 0x1ea00, v48
	ds_read_b128 v[42:45], v42
	v_or_b32_e32 v49, 0x1e800, v48
	v_or_b32_e32 v50, 0x1ec00, v48
	s_waitcnt lgkmcnt(1)
	v_cvt_pk_f16_f32 v46, v38, v39
	v_or_b32_e32 v38, 0x1e610, v48
	v_cvt_pk_f16_f32 v47, v40, v41
	ds_read_b128 v[38:41], v38
	v_or_b32_e32 v51, 0x1ea10, v48
	ds_read_b128 v[54:57], v49
	ds_read_b128 v[86:89], v50
	ds_read_b128 v[90:93], v51
	v_or_b32_e32 v94, 0x1e810, v48
	v_or_b32_e32 v48, 0x1ec10, v48
	s_waitcnt lgkmcnt(3)
	v_cvt_pk_f16_f32 v51, v38, v39
	s_waitcnt lgkmcnt(2)
	v_pk_fma_f32 v[38:39], v[54:55], 0, v[42:43] op_sel_hi:[1,0,1]
	v_cvt_pk_f16_f32 v52, v40, v41
	s_waitcnt lgkmcnt(1)
	v_pk_add_f32 v[38:39], v[86:87], v[38:39]
	v_pk_fma_f32 v[42:43], v[56:57], 0, v[44:45] op_sel_hi:[1,0,1]
	v_cvt_pk_f16_f32 v53, v38, v39
	ds_read_b128 v[38:41], v94
	ds_read_b128 v[94:97], v48
	v_pk_add_f32 v[42:43], v[88:89], v[42:43]
	s_movk_i32 s13, 0x110
	v_cvt_pk_f16_f32 v55, v42, v43
	s_waitcnt lgkmcnt(1)
	v_pk_fma_f32 v[38:39], v[38:39], 0, v[90:91] op_sel_hi:[1,0,1]
	s_or_b32 s20, s17, 0x100
	s_waitcnt lgkmcnt(0)
	v_pk_add_f32 v[38:39], v[94:95], v[38:39]
	s_or_b32 s18, s17, 0x180
	v_cvt_pk_f16_f32 v56, v38, v39
	v_pk_fma_f32 v[38:39], v[40:41], 0, v[92:93] op_sel_hi:[1,0,1]
	s_lshl_b32 s17, s14, 6
	v_pk_add_f32 v[38:39], v[96:97], v[38:39]
	v_mov_b32_e32 v122, 0x11000
	v_cvt_pk_f16_f32 v57, v38, v39
	v_mov_b32_e32 v38, v0
	s_and_b32 s5, s5, 0xffff
	v_add_u32_e32 v39, 0xffffff00, v38
	v_lshlrev_b32_e32 v38, 4, v38
	v_ashrrev_i32_e32 v39, 4, v39
	v_and_b32_e32 v40, 0xf0, v38
	v_mad_u64_u32 v[42:43], s[22:23], v39, s13, v[40:41]
	s_lshl_b32 s2, s2, 7
	s_or_b32 s2, s2, s17
	s_mov_b32 s3, 0
	s_lshr_b32 s19, s15, 6
	s_movk_i32 s21, 0x1000
	s_waitcnt vmcnt(15)
	v_pk_fma_f16 v12, v51, v12, v56
	v_pk_fma_f16 v10, v46, v10, v53
	v_pk_fma_f16 v13, v52, v13, v57
	v_pk_fma_f16 v11, v47, v11, v55
	s_waitcnt vmcnt(14)
	v_pk_fma_f16 v20, v51, v20, v56
	v_pk_fma_f16 v18, v46, v18, v53
	v_pk_fma_f16 v21, v52, v21, v57
	v_pk_fma_f16 v19, v47, v19, v55
	ds_write_b128 v42, v[10:13]
	ds_write_b128 v42, v[18:21] offset:17408
	v_pk_add_f16 v44, v13, v21
	v_pk_add_f16 v48, v12, v20
	v_pk_add_f16 v54, v11, v19
	v_pk_add_f16 v114, v10, v18
	s_waitcnt vmcnt(13)
	v_pk_fma_f16 v12, v51, v28, v56
	v_pk_fma_f16 v10, v46, v26, v53
	v_pk_fma_f16 v13, v52, v29, v57
	v_pk_fma_f16 v11, v47, v27, v55
	s_waitcnt vmcnt(10)
	v_pk_fma_f16 v20, v51, v36, v56
	v_pk_fma_f16 v18, v46, v34, v53
	v_pk_fma_f16 v21, v52, v37, v57
	v_pk_fma_f16 v19, v47, v35, v55
	ds_write_b128 v42, v[10:13] offset:4352
	ds_write_b128 v42, v[18:21] offset:21760
	v_pk_add_f16 v36, v13, v21
	v_pk_add_f16 v38, v12, v20
	v_pk_add_f16 v41, v11, v19
	v_pk_add_f16 v43, v10, v18
	v_pk_fma_f16 v12, v51, v32, v56
	v_pk_fma_f16 v10, v46, v30, v53
	v_pk_fma_f16 v13, v52, v33, v57
	v_pk_fma_f16 v11, v47, v31, v55
	s_waitcnt vmcnt(9)
	v_pk_fma_f16 v20, v51, v64, v56
	v_pk_fma_f16 v18, v46, v62, v53
	v_pk_fma_f16 v21, v52, v65, v57
	v_pk_fma_f16 v19, v47, v63, v55
	ds_write_b128 v42, v[10:13] offset:8704
	ds_write_b128 v42, v[18:21] offset:26112
	v_pk_add_f16 v30, v13, v21
	v_pk_add_f16 v31, v12, v20
	v_pk_add_f16 v33, v11, v19
	v_pk_add_f16 v35, v10, v18
	v_pk_fma_f16 v12, v51, v60, v56
	v_pk_fma_f16 v10, v46, v58, v53
	v_pk_fma_f16 v13, v52, v61, v57
	v_pk_fma_f16 v11, v47, v59, v55
	s_waitcnt vmcnt(8)
	v_pk_fma_f16 v18, v46, v66, v53
	v_pk_fma_f16 v20, v51, v68, v56
	v_pk_fma_f16 v21, v52, v69, v57
	v_pk_fma_f16 v19, v47, v67, v55
	ds_write_b128 v42, v[10:13] offset:13056
	ds_write_b128 v42, v[18:21] offset:30464
	s_waitcnt lgkmcnt(0)
	s_barrier
	v_pk_add_f16 v29, v10, v18
	v_add_u32_e32 v10, s20, v39
	v_lshl_or_b32 v18, v10, 8, v40
	v_pk_add_f16 v28, v11, v19
	v_add_u32_e32 v10, 0x1000, v18
	v_add_u32_e32 v19, 0x2000, v18
	v_pk_add_f16 v26, v13, v21
	v_pk_add_f16 v27, v12, v20
	buffer_load_dwordx4 v[60:63], v18, s[8:11], 0 offen sc1
	buffer_load_dwordx4 v[64:67], v10, s[8:11], 0 offen sc1
	v_add_u32_e32 v20, 0x3000, v18
	buffer_load_dwordx4 v[86:89], v19, s[8:11], 0 offen sc1
	buffer_load_dwordx4 v[10:13], v20, s[8:11], 0 offen sc1
	v_add_u32_e32 v19, 0x4000, v18
	v_add_u32_e32 v20, 0x5000, v18
	buffer_load_dwordx4 v[90:93], v19, s[8:11], 0 offen sc1
	buffer_load_dwordx4 v[94:97], v20, s[8:11], 0 offen sc1
	v_add_u32_e32 v32, 0x6000, v18
	v_add_u32_e32 v34, 0x7000, v18
	buffer_load_dwordx4 v[98:101], v32, s[8:11], 0 offen sc1
	buffer_load_dwordx4 v[18:21], v34, s[8:11], 0 offen sc1
	v_mov_b32_e32 v32, v0
	s_waitcnt vmcnt(15)
	v_pk_fma_f16 v72, v51, v72, v56
	v_add_u32_e32 v34, 0xffffff00, v32
	v_lshlrev_b32_e32 v32, 4, v32
	v_ashrrev_i32_e32 v59, 4, v34
	v_and_b32_e32 v102, 0xf0, v32
	v_pk_fma_f16 v70, v46, v70, v53
	v_pk_fma_f16 v73, v52, v73, v57
	v_pk_fma_f16 v71, v47, v71, v55
	s_waitcnt vmcnt(11)
	v_pk_fma_f16 v78, v46, v78, v53
	v_pk_fma_f16 v79, v47, v79, v55
	v_mad_u64_u32 v[104:105], s[22:23], v59, s13, v[102:103]
	v_pk_fma_f16 v80, v51, v80, v56
	v_pk_fma_f16 v81, v52, v81, v57
	ds_write_b128 v104, v[70:73] offset:34816
	ds_write_b128 v104, v[78:81] offset:52224
	v_pk_add_f16 v117, v71, v79
	v_pk_add_f16 v118, v70, v78
	v_pk_fma_f16 v70, v51, v76, v56
	v_pk_fma_f16 v68, v46, v74, v53
	v_pk_fma_f16 v71, v52, v77, v57
	v_pk_fma_f16 v69, v47, v75, v55
	v_pk_fma_f16 v16, v51, v16, v56
	v_pk_fma_f16 v14, v46, v14, v53
	v_pk_fma_f16 v17, v52, v17, v57
	v_pk_fma_f16 v15, v47, v15, v55
	v_pk_fma_f16 v4, v51, v4, v56
	v_pk_fma_f16 v2, v46, v2, v53
	v_pk_fma_f16 v5, v52, v5, v57
	v_pk_fma_f16 v3, v47, v3, v55
	s_waitcnt vmcnt(8)
	v_pk_fma_f16 v6, v46, v6, v53
	v_pk_add_f16 v115, v73, v81
	v_pk_add_f16 v116, v72, v80
	v_pk_fma_f16 v74, v51, v84, v56
	v_pk_fma_f16 v72, v46, v82, v53
	v_pk_fma_f16 v75, v52, v85, v57
	v_pk_fma_f16 v73, v47, v83, v55
	ds_write_b128 v104, v[68:71] offset:39168
	ds_write_b128 v104, v[72:75] offset:56576
	v_pk_fma_f16 v24, v51, v24, v56
	v_pk_fma_f16 v22, v46, v22, v53
	v_pk_fma_f16 v25, v52, v25, v57
	v_pk_fma_f16 v23, v47, v23, v55
	ds_write_b128 v104, v[14:17] offset:43520
	ds_write_b128 v104, v[22:25] offset:60928
	v_pk_fma_f16 v8, v51, v8, v56
	v_pk_fma_f16 v9, v52, v9, v57
	v_pk_fma_f16 v7, v47, v7, v55
	ds_write_b128 v104, v[2:5] offset:47872
	ds_write_b128 v104, v[6:9] offset:65280
	v_pk_add_f16 v39, v2, v6
	v_add_u32_e32 v2, s18, v59
	v_lshl_or_b32 v6, v2, 8, v102
	v_pk_add_f16 v34, v4, v8
	v_pk_add_f16 v37, v3, v7
	v_add_u32_e32 v2, 0x1000, v6
	v_add_u32_e32 v7, 0x2000, v6
	v_add_u32_e32 v8, 0x3000, v6
	v_pk_add_f16 v50, v71, v75
	v_pk_add_f16 v58, v70, v74
	v_pk_add_f16 v119, v69, v73
	v_pk_add_f16 v120, v68, v72
	v_pk_add_f16 v40, v17, v25
	v_pk_add_f16 v42, v16, v24
	v_pk_add_f16 v45, v15, v23
	v_pk_add_f16 v49, v14, v22
	v_pk_add_f16 v32, v5, v9
	buffer_load_dwordx4 v[68:71], v6, s[8:11], 0 offen sc1
	buffer_load_dwordx4 v[72:75], v2, s[8:11], 0 offen sc1
	buffer_load_dwordx4 v[14:17], v7, s[8:11], 0 offen sc1
	s_nop 0
	buffer_load_dwordx4 v[2:5], v8, s[8:11], 0 offen sc1
	v_add_u32_e32 v7, 0x4000, v6
	v_add_u32_e32 v8, 0x5000, v6
	v_add_u32_e32 v59, 0x6000, v6
	buffer_load_dwordx4 v[76:79], v7, s[8:11], 0 offen sc1
	buffer_load_dwordx4 v[80:83], v8, s[8:11], 0 offen sc1
	v_add_u32_e32 v84, 0x7000, v6
	buffer_load_dwordx4 v[22:25], v59, s[8:11], 0 offen sc1
	buffer_load_dwordx4 v[6:9], v84, s[8:11], 0 offen sc1
	v_mov_b32_e32 v59, v0
	v_fma_mix_f32 v192, v114, s44, 0 op_sel_hi:[1,0,0]
	v_fma_mix_f32 v193, v114, s44, 0 op_sel:[1,0,0] op_sel_hi:[1,0,0]
	v_fma_mix_f32 v192, v118, s44, v192 op_sel_hi:[1,0,0]
	v_fma_mix_f32 v193, v118, s44, v193 op_sel:[1,0,0] op_sel_hi:[1,0,0]
	v_fma_mix_f32 v194, v54, s44, 0 op_sel_hi:[1,0,0]
	v_fma_mix_f32 v195, v54, s44, 0 op_sel:[1,0,0] op_sel_hi:[1,0,0]
	v_fma_mix_f32 v194, v117, s44, v194 op_sel_hi:[1,0,0]
	v_fma_mix_f32 v195, v117, s44, v195 op_sel:[1,0,0] op_sel_hi:[1,0,0]
	v_fma_mix_f32 v196, v48, s44, 0 op_sel_hi:[1,0,0]
	v_fma_mix_f32 v197, v48, s44, 0 op_sel:[1,0,0] op_sel_hi:[1,0,0]
	v_fma_mix_f32 v196, v116, s44, v196 op_sel_hi:[1,0,0]
	v_fma_mix_f32 v197, v116, s44, v197 op_sel:[1,0,0] op_sel_hi:[1,0,0]
	v_fma_mix_f32 v198, v44, s44, 0 op_sel_hi:[1,0,0]
	v_fma_mix_f32 v199, v44, s44, 0 op_sel:[1,0,0] op_sel_hi:[1,0,0]
	v_fma_mix_f32 v198, v115, s44, v198 op_sel_hi:[1,0,0]
	v_fma_mix_f32 v199, v115, s44, v199 op_sel:[1,0,0] op_sel_hi:[1,0,0]
	v_fma_mix_f32 v200, v43, s44, 0 op_sel_hi:[1,0,0]
	v_fma_mix_f32 v201, v43, s44, 0 op_sel:[1,0,0] op_sel_hi:[1,0,0]
	v_fma_mix_f32 v200, v120, s44, v200 op_sel_hi:[1,0,0]
	v_fma_mix_f32 v201, v120, s44, v201 op_sel:[1,0,0] op_sel_hi:[1,0,0]
	v_fma_mix_f32 v202, v41, s44, 0 op_sel_hi:[1,0,0]
	v_fma_mix_f32 v203, v41, s44, 0 op_sel:[1,0,0] op_sel_hi:[1,0,0]
	v_fma_mix_f32 v202, v119, s44, v202 op_sel_hi:[1,0,0]
	v_fma_mix_f32 v203, v119, s44, v203 op_sel:[1,0,0] op_sel_hi:[1,0,0]
	v_fma_mix_f32 v204, v38, s44, 0 op_sel_hi:[1,0,0]
	v_fma_mix_f32 v205, v38, s44, 0 op_sel:[1,0,0] op_sel_hi:[1,0,0]
	v_fma_mix_f32 v204, v58, s44, v204 op_sel_hi:[1,0,0]
	v_fma_mix_f32 v205, v58, s44, v205 op_sel:[1,0,0] op_sel_hi:[1,0,0]
	v_fma_mix_f32 v206, v36, s44, 0 op_sel_hi:[1,0,0]
	v_fma_mix_f32 v207, v36, s44, 0 op_sel:[1,0,0] op_sel_hi:[1,0,0]
	v_fma_mix_f32 v206, v50, s44, v206 op_sel_hi:[1,0,0]
	v_fma_mix_f32 v207, v50, s44, v207 op_sel:[1,0,0] op_sel_hi:[1,0,0]
	v_fma_mix_f32 v208, v35, s44, 0 op_sel_hi:[1,0,0]
	v_fma_mix_f32 v209, v35, s44, 0 op_sel:[1,0,0] op_sel_hi:[1,0,0]
	v_fma_mix_f32 v208, v49, s44, v208 op_sel_hi:[1,0,0]
	v_fma_mix_f32 v209, v49, s44, v209 op_sel:[1,0,0] op_sel_hi:[1,0,0]
	v_fma_mix_f32 v210, v33, s44, 0 op_sel_hi:[1,0,0]
	v_fma_mix_f32 v211, v33, s44, 0 op_sel:[1,0,0] op_sel_hi:[1,0,0]
	v_fma_mix_f32 v210, v45, s44, v210 op_sel_hi:[1,0,0]
	v_fma_mix_f32 v211, v45, s44, v211 op_sel:[1,0,0] op_sel_hi:[1,0,0]
	v_fma_mix_f32 v212, v31, s44, 0 op_sel_hi:[1,0,0]
	v_fma_mix_f32 v213, v31, s44, 0 op_sel:[1,0,0] op_sel_hi:[1,0,0]
	v_fma_mix_f32 v212, v42, s44, v212 op_sel_hi:[1,0,0]
	v_fma_mix_f32 v213, v42, s44, v213 op_sel:[1,0,0] op_sel_hi:[1,0,0]
	v_fma_mix_f32 v214, v30, s44, 0 op_sel_hi:[1,0,0]
	v_fma_mix_f32 v215, v30, s44, 0 op_sel:[1,0,0] op_sel_hi:[1,0,0]
	v_fma_mix_f32 v214, v40, s44, v214 op_sel_hi:[1,0,0]
	v_fma_mix_f32 v215, v40, s44, v215 op_sel:[1,0,0] op_sel_hi:[1,0,0]
	v_fma_mix_f32 v216, v29, s44, 0 op_sel_hi:[1,0,0]
	v_fma_mix_f32 v217, v29, s44, 0 op_sel:[1,0,0] op_sel_hi:[1,0,0]
	v_fma_mix_f32 v216, v39, s44, v216 op_sel_hi:[1,0,0]
	v_fma_mix_f32 v217, v39, s44, v217 op_sel:[1,0,0] op_sel_hi:[1,0,0]
	v_fma_mix_f32 v218, v28, s44, 0 op_sel_hi:[1,0,0]
	v_fma_mix_f32 v219, v28, s44, 0 op_sel:[1,0,0] op_sel_hi:[1,0,0]
	v_fma_mix_f32 v218, v37, s44, v218 op_sel_hi:[1,0,0]
	v_fma_mix_f32 v219, v37, s44, v219 op_sel:[1,0,0] op_sel_hi:[1,0,0]
	v_fma_mix_f32 v220, v27, s44, 0 op_sel_hi:[1,0,0]
	v_fma_mix_f32 v221, v27, s44, 0 op_sel:[1,0,0] op_sel_hi:[1,0,0]
	v_fma_mix_f32 v220, v34, s44, v220 op_sel_hi:[1,0,0]
	v_fma_mix_f32 v221, v34, s44, v221 op_sel:[1,0,0] op_sel_hi:[1,0,0]
	v_fma_mix_f32 v222, v26, s44, 0 op_sel_hi:[1,0,0]
	v_fma_mix_f32 v223, v26, s44, 0 op_sel:[1,0,0] op_sel_hi:[1,0,0]
	v_fma_mix_f32 v222, v32, s44, v222 op_sel_hi:[1,0,0]
	v_fma_mix_f32 v223, v32, s44, v223 op_sel:[1,0,0] op_sel_hi:[1,0,0]
	s_waitcnt lgkmcnt(0)
	s_barrier
	s_lshl_b32 s8, s12, 16
	v_add_u32_e32 v85, 0xffffff00, v59
	v_lshlrev_b32_e32 v84, 3, v59
	v_lshrrev_b32_e32 v121, 4, v85
	v_and_b32_e32 v102, 56, v84
	v_lshrrev_b32_e32 v110, 3, v85
	s_movk_i32 s10, 0xffc0
	s_or_b32 s8, s8, s17
	v_lshl_or_b32 v84, v102, 1, v122
	s_movk_i32 s11, 0x90
	v_or_b32_e32 v106, s8, v102
	ds_read_b128 v[102:105], v162
	v_lshlrev_b32_e32 v123, 1, v106
	v_lshrrev_b32_e32 v111, 3, v59
	ds_read_b128 v[106:109], v162 offset:4608
	s_waitcnt lgkmcnt(1)
	buffer_store_dwordx4 v[102:105], v163, s[4:7], 0 offen sc1
	v_add_u32_e32 v85, 0x100, v59
	v_ashrrev_i32_e32 v85, 3, v85
	v_bfi_b32 v125, s10, v85, v110
	v_add_u32_e32 v85, 0x200, v59
	v_ashrrev_i32_e32 v85, 3, v85
	v_bfi_b32 v126, s10, v85, v111
	ds_read_b128 v[102:105], v162 offset:9216
	v_mad_u64_u32 v[84:85], s[8:9], v126, s11, v[84:85]
	ds_read_b128 v[110:113], v162 offset:13824
	s_waitcnt lgkmcnt(2)
	buffer_store_dwordx4 v[106:109], v163, s[4:7], s72 offen sc1
	s_waitcnt lgkmcnt(1)
	buffer_store_dwordx4 v[102:105], v163, s[4:7], s73 offen sc1
	v_lshlrev_b32_e32 v59, 4, v59
	s_waitcnt lgkmcnt(0)
	buffer_store_dwordx4 v[110:113], v163, s[4:7], s74 offen sc1
	v_and_b32_e32 v84, 0xf0, v59
	s_waitcnt vmcnt(19)
	v_pk_fma_f16 v63, v52, v63, v57
	v_pk_fma_f16 v62, v51, v62, v56
	v_pk_fma_f16 v61, v47, v61, v55
	v_pk_fma_f16 v60, v46, v60, v53
	s_waitcnt vmcnt(15)
	v_pk_fma_f16 v93, v52, v93, v57
	v_pk_fma_f16 v92, v51, v92, v56
	v_pk_fma_f16 v91, v47, v91, v55
	v_pk_fma_f16 v90, v46, v90, v53
	v_mad_u64_u32 v[84:85], s[8:9], v121, s13, v[84:85]
	ds_write_b128 v84, v[60:63]
	ds_write_b128 v84, v[90:93] offset:17408
	v_pk_add_f16 v59, v63, v93
	v_pk_add_f16 v85, v62, v92
	v_pk_add_f16 v91, v61, v91
	v_pk_add_f16 v90, v60, v90
	v_pk_fma_f16 v63, v52, v67, v57
	v_pk_fma_f16 v62, v51, v66, v56
	v_pk_fma_f16 v61, v47, v65, v55
	v_pk_fma_f16 v60, v46, v64, v53
	s_waitcnt vmcnt(14)
	v_pk_fma_f16 v67, v52, v97, v57
	v_pk_fma_f16 v66, v51, v96, v56
	v_pk_fma_f16 v65, v47, v95, v55
	v_pk_fma_f16 v64, v46, v94, v53
	ds_write_b128 v84, v[60:63] offset:4352
	ds_write_b128 v84, v[64:67] offset:21760
	v_pk_add_f16 v92, v63, v67
	v_pk_add_f16 v93, v62, v66
	v_pk_add_f16 v94, v61, v65
	v_pk_add_f16 v95, v60, v64
	v_pk_fma_f16 v63, v52, v89, v57
	v_pk_fma_f16 v62, v51, v88, v56
	v_pk_fma_f16 v61, v47, v87, v55
	v_pk_fma_f16 v60, v46, v86, v53
	s_waitcnt vmcnt(13)
	v_pk_fma_f16 v67, v52, v101, v57
	v_pk_fma_f16 v66, v51, v100, v56
	v_pk_fma_f16 v65, v47, v99, v55
	v_pk_fma_f16 v64, v46, v98, v53
	ds_write_b128 v84, v[60:63] offset:8704
	ds_write_b128 v84, v[64:67] offset:26112
	v_pk_add_f16 v86, v63, v67
	v_pk_add_f16 v87, v62, v66
	v_pk_add_f16 v88, v61, v65
	v_pk_add_f16 v89, v60, v64
	v_pk_fma_f16 v63, v52, v13, v57
	v_pk_fma_f16 v62, v51, v12, v56
	v_pk_fma_f16 v61, v47, v11, v55
	v_pk_fma_f16 v60, v46, v10, v53
	v_mov_b32_e32 v97, v0
	s_waitcnt vmcnt(12)
	v_pk_fma_f16 v21, v52, v21, v57
	v_pk_fma_f16 v20, v51, v20, v56
	v_pk_fma_f16 v19, v47, v19, v55
	v_pk_fma_f16 v18, v46, v18, v53
	ds_write_b128 v84, v[60:63] offset:13056
	ds_write_b128 v84, v[18:21] offset:30464
	s_waitcnt lgkmcnt(0)
	s_barrier
	v_pk_add_f16 v96, v60, v18
	v_add_u32_e32 v13, 0xffffff00, v97
	v_lshlrev_b32_e32 v12, 3, v97
	v_lshrrev_b32_e32 v98, 4, v13
	v_and_b32_e32 v18, 56, v12
	v_lshrrev_b32_e32 v64, 3, v13
	v_lshl_or_b32 v12, v18, 1, v122
	v_pk_add_f16 v84, v61, v19
	v_or_b32_e32 v60, s2, v18
	v_pk_add_f16 v10, v63, v21
	v_pk_add_f16 v11, v62, v20
	ds_read_b128 v[18:21], v162 offset:18432
	v_lshlrev_b32_e32 v99, 1, v60
	v_lshrrev_b32_e32 v65, 3, v97
	v_ashrrev_i32_e32 v60, 3, v97
	v_bfi_b32 v66, s10, v60, v65
	ds_read_b128 v[60:63], v162 offset:23040
	s_waitcnt lgkmcnt(1)
	buffer_store_dwordx4 v[18:21], v163, s[4:7], s75 offen sc1
	v_add_u32_e32 v13, 0x100, v97
	v_ashrrev_i32_e32 v13, 3, v13
	v_bfi_b32 v101, s10, v13, v64
	v_add_u32_e32 v13, 0x200, v97
	v_ashrrev_i32_e32 v13, 3, v13
	v_bfi_b32 v102, s10, v13, v65
	ds_read_b128 v[18:21], v162 offset:27648
	v_mad_u64_u32 v[12:13], s[8:9], v102, s11, v[12:13]
	v_lshl_add_u32 v100, v66, 8, v99
	ds_read_b128 v[64:67], v162 offset:32256
	s_waitcnt lgkmcnt(2)
	buffer_store_dwordx4 v[60:63], v163, s[4:7], s76 offen sc1
	s_waitcnt lgkmcnt(1)
	buffer_store_dwordx4 v[18:21], v163, s[4:7], s77 offen sc1
	s_waitcnt lgkmcnt(0)
	buffer_store_dwordx4 v[64:67], v163, s[4:7], s78 offen sc1
	v_lshlrev_b32_e32 v12, 4, v97
	v_and_b32_e32 v12, 0xf0, v12
	s_waitcnt vmcnt(15)
	v_pk_fma_f16 v21, v52, v71, v57
	v_pk_fma_f16 v20, v51, v70, v56
	v_pk_fma_f16 v19, v47, v69, v55
	v_pk_fma_f16 v18, v46, v68, v53
	s_waitcnt vmcnt(11)
	v_pk_fma_f16 v63, v52, v79, v57
	v_pk_fma_f16 v62, v51, v78, v56
	v_pk_fma_f16 v61, v47, v77, v55
	v_pk_fma_f16 v60, v46, v76, v53
	v_mad_u64_u32 v[12:13], s[8:9], v98, s13, v[12:13]
	ds_write_b128 v12, v[18:21] offset:34816
	ds_write_b128 v12, v[60:63] offset:52224
	v_pk_add_f16 v13, v21, v63
	v_pk_add_f16 v64, v20, v62
	v_pk_add_f16 v65, v19, v61
	v_pk_add_f16 v66, v18, v60
	v_pk_fma_f16 v21, v52, v75, v57
	v_pk_fma_f16 v20, v51, v74, v56
	v_pk_fma_f16 v19, v47, v73, v55
	v_pk_fma_f16 v18, v46, v72, v53
	s_waitcnt vmcnt(10)
	v_pk_fma_f16 v63, v52, v83, v57
	v_pk_fma_f16 v62, v51, v82, v56
	v_pk_fma_f16 v61, v47, v81, v55
	v_pk_fma_f16 v60, v46, v80, v53
	v_pk_fma_f16 v17, v52, v17, v57
	v_pk_fma_f16 v16, v51, v16, v56
	v_pk_fma_f16 v15, v47, v15, v55
	v_pk_fma_f16 v14, v46, v14, v53
	v_pk_fma_f16 v5, v52, v5, v57
	v_pk_fma_f16 v4, v51, v4, v56
	v_pk_fma_f16 v3, v47, v3, v55
	v_pk_fma_f16 v2, v46, v2, v53
	s_waitcnt vmcnt(8)
	v_pk_fma_f16 v7, v47, v7, v55
	v_pk_fma_f16 v6, v46, v6, v53
	ds_write_b128 v12, v[18:21] offset:39168
	ds_write_b128 v12, v[60:63] offset:56576
	v_pk_add_f16 v63, v21, v63
	v_pk_add_f16 v62, v20, v62
	v_pk_add_f16 v61, v19, v61
	v_pk_add_f16 v60, v18, v60
	v_pk_fma_f16 v21, v52, v25, v57
	v_pk_fma_f16 v20, v51, v24, v56
	v_pk_fma_f16 v19, v47, v23, v55
	v_pk_fma_f16 v18, v46, v22, v53
	ds_write_b128 v12, v[14:17] offset:43520
	ds_write_b128 v12, v[18:21] offset:60928
	v_pk_fma_f16 v9, v52, v9, v57
	v_pk_fma_f16 v8, v51, v8, v56
	ds_write_b128 v12, v[2:5] offset:47872
	ds_write_b128 v12, v[6:9] offset:65280
	v_pk_add_f16 v24, v3, v7
	v_pk_add_f16 v25, v2, v6
	v_pk_add_f16 v22, v5, v9
	v_pk_add_f16 v23, v4, v8
	v_fma_mix_f32 v192, v90, s44, v192 op_sel_hi:[1,0,0]
	v_fma_mix_f32 v193, v90, s44, v193 op_sel:[1,0,0] op_sel_hi:[1,0,0]
	v_fma_mixlo_f16 v224, v66, s44, v192 op_sel_hi:[1,0,0]
	s_nop 0
	v_fma_mixhi_f16 v224, v66, s44, v193 op_sel:[1,0,0] op_sel_hi:[1,0,0]
	v_pk_add_f16 v19, v15, v19
	v_fma_mix_f32 v194, v91, s44, v194 op_sel_hi:[1,0,0]
	v_fma_mix_f32 v195, v91, s44, v195 op_sel:[1,0,0] op_sel_hi:[1,0,0]
	v_pk_add_f16 v18, v14, v18
	v_fma_mixlo_f16 v225, v65, s44, v194 op_sel_hi:[1,0,0]
	s_nop 0
	v_fma_mixhi_f16 v225, v65, s44, v195 op_sel:[1,0,0] op_sel_hi:[1,0,0]
	s_mov_b32 s2, 0x3e000000
	v_fma_mix_f32 v196, v85, s44, v196 op_sel_hi:[1,0,0]
	v_fma_mix_f32 v197, v85, s44, v197 op_sel:[1,0,0] op_sel_hi:[1,0,0]
	v_fma_mixlo_f16 v226, v64, s44, v196 op_sel_hi:[1,0,0]
	s_nop 0
	v_fma_mixhi_f16 v226, v64, s44, v197 op_sel:[1,0,0] op_sel_hi:[1,0,0]
	v_pk_add_f16 v21, v17, v21
	v_fma_mix_f32 v198, v59, s44, v198 op_sel_hi:[1,0,0]
	v_fma_mix_f32 v199, v59, s44, v199 op_sel:[1,0,0] op_sel_hi:[1,0,0]
	v_pk_add_f16 v20, v16, v20
	v_fma_mixlo_f16 v227, v13, s44, v198 op_sel_hi:[1,0,0]
	s_nop 0
	v_fma_mixhi_f16 v227, v13, s44, v199 op_sel:[1,0,0] op_sel_hi:[1,0,0]
	v_fma_mix_f32 v200, v60, s44, v200 op_sel_hi:[1,0,0]
	v_add_u32_e32 v16, 0x1a000, v12
	v_fma_mix_f32 v201, v60, s44, v201 op_sel:[1,0,0] op_sel_hi:[1,0,0]
	ds_write_b128 v16, v[224:227]
	v_fma_mixlo_f16 v228, v95, s44, v200 op_sel_hi:[1,0,0]
	s_nop 0
	v_fma_mixhi_f16 v228, v95, s44, v201 op_sel:[1,0,0] op_sel_hi:[1,0,0]
	v_fma_mix_f32 v202, v61, s44, v202 op_sel_hi:[1,0,0]
	s_nop 0
	v_fma_mixlo_f16 v229, v94, s44, v202 op_sel_hi:[1,0,0]
	v_fma_mix_f32 v203, v94, s44, v203 op_sel:[1,0,0] op_sel_hi:[1,0,0]
	v_fma_mixhi_f16 v229, v61, s44, v203 op_sel:[1,0,0] op_sel_hi:[1,0,0]
	v_fma_mix_f32 v204, v93, s44, v204 op_sel_hi:[1,0,0]
	v_fma_mix_f32 v205, v93, s44, v205 op_sel:[1,0,0] op_sel_hi:[1,0,0]
	v_fma_mixlo_f16 v230, v62, s44, v204 op_sel_hi:[1,0,0]
	s_nop 0
	v_fma_mixhi_f16 v230, v62, s44, v205 op_sel:[1,0,0] op_sel_hi:[1,0,0]
	v_fma_mix_f32 v206, v63, s44, v206 op_sel_hi:[1,0,0]
	s_nop 0
	v_fma_mixlo_f16 v231, v92, s44, v206 op_sel_hi:[1,0,0]
	v_fma_mix_f32 v207, v92, s44, v207 op_sel:[1,0,0] op_sel_hi:[1,0,0]
	v_fma_mixhi_f16 v231, v63, s44, v207 op_sel:[1,0,0] op_sel_hi:[1,0,0]
	v_fma_mix_f32 v208, v18, s44, v208 op_sel_hi:[1,0,0]
	v_fma_mix_f32 v209, v18, s44, v209 op_sel:[1,0,0] op_sel_hi:[1,0,0]
	v_fma_mix_f32 v210, v19, s44, v210 op_sel_hi:[1,0,0]
	ds_write_b128 v16, v[228:231] offset:4352
	v_fma_mixlo_f16 v232, v89, s44, v208 op_sel_hi:[1,0,0]
	s_nop 0
	v_fma_mixhi_f16 v232, v89, s44, v209 op_sel:[1,0,0] op_sel_hi:[1,0,0]
	v_fma_mix_f32 v211, v19, s44, v211 op_sel:[1,0,0] op_sel_hi:[1,0,0]
	v_fma_mixlo_f16 v233, v88, s44, v210 op_sel_hi:[1,0,0]
	s_nop 0
	v_fma_mixhi_f16 v233, v88, s44, v211 op_sel:[1,0,0] op_sel_hi:[1,0,0]
	v_fma_mix_f32 v212, v87, s44, v212 op_sel_hi:[1,0,0]
	v_fma_mix_f32 v213, v87, s44, v213 op_sel:[1,0,0] op_sel_hi:[1,0,0]
	v_fma_mixlo_f16 v234, v20, s44, v212 op_sel_hi:[1,0,0]
	s_nop 0
	v_fma_mixhi_f16 v234, v20, s44, v213 op_sel:[1,0,0] op_sel_hi:[1,0,0]
	v_fma_mix_f32 v214, v21, s44, v214 op_sel_hi:[1,0,0]
	s_nop 0
	v_fma_mixlo_f16 v235, v86, s44, v214 op_sel_hi:[1,0,0]
	v_fma_mix_f32 v215, v86, s44, v215 op_sel:[1,0,0] op_sel_hi:[1,0,0]
	v_fma_mixhi_f16 v235, v21, s44, v215 op_sel:[1,0,0] op_sel_hi:[1,0,0]
	v_fma_mix_f32 v216, v25, s44, v216 op_sel_hi:[1,0,0]
	v_fma_mix_f32 v217, v25, s44, v217 op_sel:[1,0,0] op_sel_hi:[1,0,0]
	v_fma_mix_f32 v218, v24, s44, v218 op_sel_hi:[1,0,0]
	ds_write_b128 v16, v[232:235] offset:8704
	v_fma_mixlo_f16 v236, v96, s44, v216 op_sel_hi:[1,0,0]
	s_nop 0
	v_fma_mixhi_f16 v236, v96, s44, v217 op_sel:[1,0,0] op_sel_hi:[1,0,0]
	v_fma_mix_f32 v219, v24, s44, v219 op_sel:[1,0,0] op_sel_hi:[1,0,0]
	v_fma_mixlo_f16 v237, v84, s44, v218 op_sel_hi:[1,0,0]
	s_nop 0
	v_fma_mixhi_f16 v237, v84, s44, v219 op_sel:[1,0,0] op_sel_hi:[1,0,0]
	v_fma_mix_f32 v220, v11, s44, v220 op_sel_hi:[1,0,0]
	v_fma_mix_f32 v221, v11, s44, v221 op_sel:[1,0,0] op_sel_hi:[1,0,0]
	v_fma_mixlo_f16 v238, v23, s44, v220 op_sel_hi:[1,0,0]
	s_nop 0
	v_fma_mixhi_f16 v238, v23, s44, v221 op_sel:[1,0,0] op_sel_hi:[1,0,0]
	v_fma_mix_f32 v223, v22, s44, v223 op_sel:[1,0,0] op_sel_hi:[1,0,0]
	v_fma_mix_f32 v222, v10, s44, v222 op_sel_hi:[1,0,0]
	v_fma_mixhi_f16 v239, v10, s44, v223 op_sel:[1,0,0] op_sel_hi:[1,0,0]
	s_nop 0
	v_fma_mixlo_f16 v239, v22, s44, v222 op_sel_hi:[1,0,0]
	s_cmpk_lt_u32 s15, 0x180
	s_cselect_b64 s[8:9], -1, 0
	s_cmpk_gt_u32 s15, 0x17f
	ds_write_b128 v16, v[236:239] offset:13056
	s_cbranch_scc1 .LBB2_3
	s_load_dwordx2 s[10:11], s[0:1], 0x78
	s_load_dwordx4 s[24:27], s[0:1], 0x50
	v_mov_b32_e32 v2, v0
	s_ashr_i32 s13, s12, 31
	s_lshl_b64 s[22:23], s[12:13], 12
	s_waitcnt lgkmcnt(0)
	s_add_u32 s10, s10, s22
	v_lshlrev_b32_e32 v2, 3, v2
	s_addc_u32 s11, s11, s23
	v_and_b32_e32 v2, 0x1f8, v2
	global_load_dwordx2 v[136:137], v2, s[10:11]
	global_load_dwordx2 v[132:133], v2, s[10:11] offset:512
	global_load_dwordx2 v[128:129], v2, s[10:11] offset:1024
	global_load_dwordx2 v[124:125], v2, s[10:11] offset:1536
	global_load_dwordx2 v[134:135], v2, s[10:11] offset:2048
	global_load_dwordx2 v[130:131], v2, s[10:11] offset:2560
	global_load_dwordx2 v[126:127], v2, s[10:11] offset:3072
	global_load_dwordx2 v[122:123], v2, s[10:11] offset:3584
	s_lshl_b32 s2, s14, 4
	s_lshl_b32 s10, s19, 3
	s_add_i32 s10, s10, s2
	s_sub_i32 s2, s10, 32
	s_lshl_b64 s[2:3], s[2:3], 10
	v_lshl_or_b32 v2, v2, 1, s2
	v_mov_b32_e32 v3, s3
	v_lshl_add_u64 v[4:5], s[24:25], 0, v[2:3]
	global_load_dwordx4 v[18:21], v[4:5], off
	global_load_dwordx4 v[102:105], v[4:5], off offset:1024
	global_load_dwordx4 v[94:97], v[4:5], off offset:2048
	global_load_dwordx4 v[86:89], v[4:5], off offset:3072
	v_add_co_u32_e32 v4, vcc, s21, v4
	v_lshl_add_u64 v[6:7], s[26:27], 0, v[2:3]
	s_nop 0
	v_addc_co_u32_e32 v5, vcc, 0, v5, vcc
	global_load_dwordx4 v[78:81], v[4:5], off
	global_load_dwordx4 v[74:77], v[4:5], off offset:1024
	global_load_dwordx4 v[70:73], v[4:5], off offset:2048
	global_load_dwordx4 v[66:69], v[4:5], off offset:3072
	s_nop 0
	global_load_dwordx4 v[2:5], v[6:7], off
	global_load_dwordx4 v[118:121], v[6:7], off offset:1024
	global_load_dwordx4 v[114:117], v[6:7], off offset:2048
	global_load_dwordx4 v[110:113], v[6:7], off offset:3072
	v_add_co_u32_e32 v6, vcc, s21, v6
	s_nop 1
	v_addc_co_u32_e32 v7, vcc, 0, v7, vcc
	global_load_dwordx4 v[106:109], v[6:7], off
	global_load_dwordx4 v[98:101], v[6:7], off offset:1024
	global_load_dwordx4 v[90:93], v[6:7], off offset:2048
	global_load_dwordx4 v[82:85], v[6:7], off offset:3072
	s_branch .LBB2_4

.LBB2_10:
	v_mov_b32_e32 v11, v0
	s_waitcnt lgkmcnt(0)
	s_barrier
	s_lshl_b32 s8, s18, 7
	s_waitcnt vmcnt(7)
	ds_read_b128 v[2:5], v162 offset:18432
	ds_read_b128 v[6:9], v162 offset:23040
	ds_read_b128 v[10:13], v162 offset:27648
	ds_read_b128 v[14:17], v162 offset:32256
	s_waitcnt lgkmcnt(3)
	buffer_store_dwordx4 v[2:5], v163, s[4:7], s66 offen sc1
	s_waitcnt lgkmcnt(2)
	buffer_store_dwordx4 v[6:9], v163, s[4:7], s67 offen sc1
	s_waitcnt lgkmcnt(1)
	buffer_store_dwordx4 v[10:13], v163, s[4:7], s68 offen sc1
	s_waitcnt lgkmcnt(0)
	buffer_store_dwordx4 v[14:17], v163, s[4:7], s69 offen sc1
	s_movk_i32 s4, 0x13f
	v_cmp_lt_u32_e32 vcc, s4, v0
	s_and_saveexec_b64 s[4:5], vcc
	s_xor_b64 s[4:5], exec, s[4:5]
	s_cbranch_execz .LBB2_14
	s_movk_i32 s6, 0x180
	v_cmp_gt_u32_e32 vcc, s6, v0
	s_and_saveexec_b64 s[6:7], vcc
	s_cbranch_execz .LBB2_13
	v_mov_b32_e32 v2, 0x1e400
	v_lshl_add_u32 v1, v1, 2, v2
	s_lshl_b32 s8, s16, 8
	ds_read_b32 v1, v1
	s_or_b32 s8, s17, s8
	v_add_u32_e32 v2, s8, v0
	v_add_u32_e32 v2, 0xffffff40, v2
	v_mov_b32_e32 v3, 0
	v_lshl_add_u64 v[2:3], v[2:3], 2, s[2:3]
	s_waitcnt lgkmcnt(0)
	global_atomic_add_f32 v[2:3], v1, off

_Z7k_layerILi0EEvPKDF16_S1_PKfS3_S3_S3_S3_S3_S1_S1_S1_S1_S3_S3_PKhS5_PDF16_S6_PfS7_:
	s_ashr_i32 s3, s2, 1
	s_and_b32 s3, s3, -8
	s_and_b32 s16, s2, 7
	v_readfirstlane_b32 s15, v0
	s_or_b32 s12, s3, s16
	s_bfe_u32 s14, s2, 0x10003
	s_cmpk_gt_u32 s15, 0xff
	s_mov_b64 s[2:3], -1
	s_cbranch_scc0 .LBB3_17
	s_mov_b32 s72, 0x2000
	s_mov_b32 s73, 0x4000
	s_mov_b32 s74, 0x6000
	s_mov_b32 s75, 0x8000
	s_mov_b32 s76, 0xa000
	s_mov_b32 s77, 0xc000
	s_mov_b32 s78, 0xe000
	s_lshl_b32 s70, s12, 17
	s_lshl_b32 s66, s14, 7
	s_or_b32 s70, s70, s66
	s_mov_b32 s66, 0x18000
	s_mov_b32 s67, 0x1a000
	s_mov_b32 s68, 0x1c000
	s_mov_b32 s69, 0x1e000
	v_add_u32_e32 v165, 0xffffff00, v0
	v_lshrrev_b32_e32 v163, 3, v165
	v_and_b32_e32 v165, 7, v165
	v_lshlrev_b32_e32 v165, 4, v165
	v_mul_u32_u24_e32 v162, 0x90, v163
	v_add_u32_e32 v162, v162, v165
	v_add_u32_e32 v162, 0x11000, v162
	v_lshl_add_u32 v163, v163, 8, v165
	v_add_u32_e32 v163, s70, v163
	s_mov_b32 s44, 0x3e000000
	v_mov_b32_e32 v240, 0x64646464
	s_mov_b32 s42, 0x4010400
	s_mov_b32 s43, 0x4030402
	s_load_dwordx4 s[8:11], s[0:1], 0x0
	s_load_dwordx2 s[4:5], s[0:1], 0x80
	v_add_u32_e32 v1, 0xffffff00, v0
	s_ashr_i32 s13, s12, 31
	s_lshr_b32 s17, s15, 6
	v_ashrrev_i32_e32 v2, 4, v1
	v_lshlrev_b32_e32 v3, 3, v0
	s_lshl_b64 s[2:3], s[12:13], 14
	v_and_b32_e32 v82, 0x78, v3
	v_ashrrev_i32_e32 v3, 31, v2
	s_waitcnt lgkmcnt(0)
	s_add_u32 s2, s10, s2
	s_addc_u32 s3, s11, s3
	v_lshlrev_b64 v[4:5], 8, v[2:3]
	v_lshl_add_u64 v[4:5], s[2:3], 0, v[4:5]
	v_lshlrev_b32_e32 v6, 1, v82
	v_mov_b32_e32 v7, 0
	v_lshl_add_u64 v[4:5], v[4:5], 0, v[6:7]
	s_movk_i32 s2, 0x2000
	v_add_co_u32_e32 v8, vcc, s2, v4
	global_load_dwordx4 v[74:77], v[4:5], off
	s_nop 0
	v_addc_co_u32_e32 v9, vcc, 0, v5, vcc
	global_load_dwordx4 v[78:81], v[8:9], off offset:-4096
	global_load_dwordx4 v[66:69], v[8:9], off
	s_movk_i32 s2, 0x3000
	v_add_co_u32_e32 v4, vcc, s2, v4
	s_lshl_b32 s18, s12, 9
	s_nop 0
	v_addc_co_u32_e32 v5, vcc, 0, v5, vcc
	global_load_dwordx4 v[62:65], v[4:5], off
	v_add_u32_e32 v3, s18, v2
	s_mov_b32 s7, 0x20000
	s_mov_b32 s6, 0x1000000
	v_lshl_or_b32 v3, v3, 8, v6
	s_and_b32 s9, s9, 0xffff
	s_mov_b32 s10, s6
	s_mov_b32 s11, s7
	v_add_u32_e32 v4, 0x1000, v3
	buffer_load_dwordx4 v[58:61], v3, s[8:11], 0 offen sc1
	buffer_load_dwordx4 v[50:53], v4, s[8:11], 0 offen sc1
	v_add_u32_e32 v4, 0x2000, v3
	v_add_u32_e32 v5, 0x3000, v3
	buffer_load_dwordx4 v[42:45], v4, s[8:11], 0 offen sc1
	buffer_load_dwordx4 v[34:37], v5, s[8:11], 0 offen sc1
	v_add_u32_e32 v4, 0x4000, v3
	v_add_u32_e32 v5, 0x5000, v3
	buffer_load_dwordx4 v[70:73], v4, s[8:11], 0 offen sc1
	buffer_load_dwordx4 v[54:57], v5, s[8:11], 0 offen sc1
	v_add_u32_e32 v4, 0x6000, v3
	v_add_u32_e32 v3, 0x7000, v3
	buffer_load_dwordx4 v[46:49], v4, s[8:11], 0 offen sc1
	buffer_load_dwordx4 v[38:41], v3, s[8:11], 0 offen sc1
	s_or_b32 s2, s18, 0x80
	v_add_u32_e32 v2, s2, v2
	v_lshl_or_b32 v6, v2, 8, v6
	v_add_u32_e32 v2, 0x1000, v6
	v_add_u32_e32 v7, 0x2000, v6
	v_add_u32_e32 v8, 0x3000, v6
	buffer_load_dwordx4 v[26:29], v6, s[8:11], 0 offen sc1
	buffer_load_dwordx4 v[18:21], v2, s[8:11], 0 offen sc1
	buffer_load_dwordx4 v[10:13], v7, s[8:11], 0 offen sc1
	s_nop 0
	buffer_load_dwordx4 v[2:5], v8, s[8:11], 0 offen sc1
	v_add_u32_e32 v7, 0x4000, v6
	v_add_u32_e32 v8, 0x5000, v6
	v_add_u32_e32 v83, 0x6000, v6
	buffer_load_dwordx4 v[30:33], v7, s[8:11], 0 offen sc1
	buffer_load_dwordx4 v[22:25], v8, s[8:11], 0 offen sc1
	v_add_u32_e32 v84, 0x7000, v6
	buffer_load_dwordx4 v[14:17], v83, s[8:11], 0 offen sc1
	buffer_load_dwordx4 v[6:9], v84, s[8:11], 0 offen sc1
	v_lshlrev_b32_e32 v92, 2, v82
	v_or_b32_e32 v82, 0x1e600, v92
	s_barrier
	ds_read_b128 v[82:85], v82
	v_or_b32_e32 v86, 0x1ea00, v92
	ds_read_b128 v[88:91], v86
	v_or_b32_e32 v93, 0x1e800, v92
	v_or_b32_e32 v102, 0x1ec00, v92
	s_waitcnt lgkmcnt(1)
	v_cvt_pk_f16_f32 v82, v82, v83
	v_cvt_pk_f16_f32 v83, v84, v85
	v_or_b32_e32 v84, 0x1e610, v92
	ds_read_b128 v[84:87], v84
	v_or_b32_e32 v94, 0x1ea10, v92
	v_or_b32_e32 v108, 0x1e810, v92
	v_or_b32_e32 v109, 0x1ec10, v92
	ds_read_b128 v[94:97], v94
	ds_read_b128 v[98:101], v93
	ds_read_b128 v[102:105], v102
	s_waitcnt lgkmcnt(3)
	v_cvt_pk_f16_f32 v84, v84, v85
	s_movk_i32 s22, 0x110
	s_or_b32 s21, s18, 0x100
	s_or_b32 s19, s18, 0x180
	v_mov_b32_e32 v130, v0
	s_lshl_b32 s18, s14, 6
	v_mov_b32_e32 v132, 0x11000
	s_and_b32 s5, s5, 0xffff
	s_lshl_b32 s2, s2, 7
	s_or_b32 s2, s2, s18
	s_mov_b32 s3, 0
	s_movk_i32 s20, 0x1000
	s_waitcnt vmcnt(19)
	v_cvt_f32_f16_e32 v92, v74
	v_cvt_f32_f16_sdwa v93, v74 dst_sel:DWORD dst_unused:UNUSED_PAD src0_sel:WORD_1
	s_waitcnt vmcnt(18)
	v_cvt_f32_f16_e32 v106, v78
	v_cvt_f32_f16_sdwa v107, v78 dst_sel:DWORD dst_unused:UNUSED_PAD src0_sel:WORD_1
	v_cvt_pk_f16_f32 v74, v86, v87
	s_waitcnt lgkmcnt(1)
	v_pk_fma_f32 v[86:87], v[98:99], v[92:93], v[88:89]
	v_pk_fma_f32 v[92:93], v[98:99], v[106:107], v[88:89]
	s_waitcnt lgkmcnt(0)
	v_pk_add_f32 v[92:93], v[102:103], v[92:93]
	s_waitcnt vmcnt(17)
	v_cvt_f32_f16_e32 v106, v66
	v_cvt_f32_f16_sdwa v107, v66 dst_sel:DWORD dst_unused:UNUSED_PAD src0_sel:WORD_1
	v_cvt_pk_f16_f32 v85, v92, v93
	s_waitcnt vmcnt(16)
	v_cvt_f32_f16_e32 v92, v62
	v_cvt_f32_f16_sdwa v93, v62 dst_sel:DWORD dst_unused:UNUSED_PAD src0_sel:WORD_1
	v_cvt_f32_f16_e32 v66, v67
	v_cvt_f32_f16_sdwa v67, v67 dst_sel:DWORD dst_unused:UNUSED_PAD src0_sel:WORD_1
	v_cvt_f32_f16_e32 v62, v63
	v_cvt_f32_f16_sdwa v63, v63 dst_sel:DWORD dst_unused:UNUSED_PAD src0_sel:WORD_1
	v_pk_fma_f32 v[106:107], v[98:99], v[106:107], v[88:89]
	v_pk_fma_f32 v[88:89], v[98:99], v[92:93], v[88:89]
	v_cvt_f32_f16_e32 v92, v75
	v_cvt_f32_f16_sdwa v93, v75 dst_sel:DWORD dst_unused:UNUSED_PAD src0_sel:WORD_1
	v_cvt_f32_f16_e32 v98, v79
	v_cvt_f32_f16_sdwa v99, v79 dst_sel:DWORD dst_unused:UNUSED_PAD src0_sel:WORD_1
	v_pk_add_f32 v[88:89], v[102:103], v[88:89]
	v_pk_fma_f32 v[66:67], v[100:101], v[66:67], v[90:91]
	v_pk_fma_f32 v[62:63], v[100:101], v[62:63], v[90:91]
	v_cvt_pk_f16_f32 v75, v88, v89
	v_pk_fma_f32 v[88:89], v[100:101], v[92:93], v[90:91]
	v_pk_fma_f32 v[92:93], v[100:101], v[98:99], v[90:91]
	v_pk_add_f32 v[66:67], v[104:105], v[66:67]
	v_pk_add_f32 v[62:63], v[104:105], v[62:63]
	v_pk_add_f32 v[86:87], v[102:103], v[86:87]
	v_pk_add_f32 v[106:107], v[102:103], v[106:107]
	v_pk_add_f32 v[88:89], v[104:105], v[88:89]
	v_pk_add_f32 v[92:93], v[104:105], v[92:93]
	v_cvt_pk_f16_f32 v79, v66, v67
	ds_read_b128 v[98:101], v108
	ds_read_b128 v[102:105], v109
	v_cvt_f32_f16_e32 v66, v76
	v_cvt_f32_f16_sdwa v67, v76 dst_sel:DWORD dst_unused:UNUSED_PAD src0_sel:WORD_1
	v_cvt_pk_f16_f32 v76, v62, v63
	v_cvt_f32_f16_e32 v62, v80
	v_cvt_f32_f16_sdwa v63, v80 dst_sel:DWORD dst_unused:UNUSED_PAD src0_sel:WORD_1
	s_waitcnt lgkmcnt(1)
	v_pk_fma_f32 v[66:67], v[98:99], v[66:67], v[94:95]
	v_cvt_pk_f16_f32 v87, v86, v87
	s_waitcnt lgkmcnt(0)
	v_pk_add_f32 v[66:67], v[102:103], v[66:67]
	v_pk_fma_f32 v[62:63], v[98:99], v[62:63], v[94:95]
	v_cvt_pk_f16_f32 v88, v88, v89
	v_pk_add_f32 v[62:63], v[102:103], v[62:63]
	v_cvt_pk_f16_f32 v86, v92, v93
	v_cvt_pk_f16_f32 v92, v66, v67
	v_cvt_f32_f16_e32 v66, v68
	v_cvt_f32_f16_sdwa v67, v68 dst_sel:DWORD dst_unused:UNUSED_PAD src0_sel:WORD_1
	v_cvt_pk_f16_f32 v89, v62, v63
	v_cvt_f32_f16_e32 v62, v64
	v_cvt_f32_f16_sdwa v63, v64 dst_sel:DWORD dst_unused:UNUSED_PAD src0_sel:WORD_1
	v_pk_fma_f32 v[66:67], v[98:99], v[66:67], v[94:95]
	v_cvt_pk_f16_f32 v78, v106, v107
	v_pk_add_f32 v[66:67], v[102:103], v[66:67]
	v_pk_fma_f32 v[62:63], v[98:99], v[62:63], v[94:95]
	v_cvt_pk_f16_f32 v80, v66, v67
	v_pk_add_f32 v[62:63], v[102:103], v[62:63]
	v_cvt_f32_f16_e32 v66, v77
	v_cvt_f32_f16_sdwa v67, v77 dst_sel:DWORD dst_unused:UNUSED_PAD src0_sel:WORD_1
	v_cvt_pk_f16_f32 v77, v62, v63
	v_cvt_f32_f16_e32 v62, v81
	v_cvt_f32_f16_sdwa v63, v81 dst_sel:DWORD dst_unused:UNUSED_PAD src0_sel:WORD_1
	v_pk_fma_f32 v[66:67], v[100:101], v[66:67], v[96:97]
	s_waitcnt vmcnt(15)
	v_pk_fma_f16 v59, v83, v59, v88
	v_pk_add_f32 v[66:67], v[104:105], v[66:67]
	v_pk_fma_f32 v[62:63], v[100:101], v[62:63], v[96:97]
	v_cvt_pk_f16_f32 v95, v66, v67
	v_pk_add_f32 v[62:63], v[104:105], v[62:63]
	v_cvt_f32_f16_e32 v66, v69
	v_cvt_pk_f16_f32 v93, v62, v63
	v_cvt_f32_f16_e32 v62, v65
	v_cvt_f32_f16_sdwa v63, v65 dst_sel:DWORD dst_unused:UNUSED_PAD src0_sel:WORD_1
	v_cvt_f32_f16_sdwa v67, v69 dst_sel:DWORD dst_unused:UNUSED_PAD src0_sel:WORD_1
	v_pk_fma_f16 v61, v74, v61, v95
	v_pk_fma_f16 v58, v82, v58, v87
	v_pk_fma_f32 v[62:63], v[100:101], v[62:63], v[96:97]
	v_pk_fma_f32 v[64:65], v[100:101], v[66:67], v[96:97]
	v_pk_add_f32 v[62:63], v[104:105], v[62:63]
	v_pk_add_f32 v[64:65], v[104:105], v[64:65]
	v_cvt_pk_f16_f32 v81, v62, v63
	v_mov_b32_e32 v62, v0
	v_cvt_pk_f16_f32 v91, v64, v65
	v_add_u32_e32 v63, 0xffffff00, v62
	v_lshlrev_b32_e32 v62, 4, v62
	v_ashrrev_i32_e32 v94, 4, v63
	v_and_b32_e32 v90, 0xf0, v62
	v_pk_fma_f16 v60, v84, v60, v92
	s_waitcnt vmcnt(11)
	v_pk_fma_f16 v62, v82, v70, v87
	v_pk_fma_f16 v51, v83, v51, v86
	v_pk_fma_f16 v53, v74, v53, v93
	v_pk_fma_f16 v50, v82, v50, v85
	v_pk_fma_f16 v52, v84, v52, v89
	v_pk_fma_f16 v43, v83, v43, v79
	v_pk_fma_f16 v45, v74, v45, v91
	v_pk_fma_f16 v42, v82, v42, v78
	v_pk_fma_f16 v44, v84, v44, v80
	v_pk_fma_f16 v35, v83, v35, v76
	v_pk_fma_f16 v37, v74, v37, v81
	v_pk_fma_f16 v34, v82, v34, v75
	v_pk_fma_f16 v36, v84, v36, v77
	s_waitcnt vmcnt(8)
	v_pk_fma_f16 v38, v82, v38, v75
	v_pk_fma_f16 v63, v83, v71, v88
	v_pk_fma_f16 v65, v74, v73, v95
	v_pk_fma_f16 v64, v84, v72, v92
	v_pk_max_f16 v60, v60, 0
	v_pk_max_f16 v58, v58, 0
	v_pk_max_f16 v61, v61, 0
	v_pk_max_f16 v59, v59, 0
	v_pk_max_f16 v62, v62, 0
	v_mad_u64_u32 v[96:97], s[24:25], v94, s22, v[90:91]
	v_pk_fma_f16 v55, v83, v55, v86
	v_pk_fma_f16 v57, v74, v57, v93
	v_pk_fma_f16 v54, v82, v54, v85
	v_pk_fma_f16 v56, v84, v56, v89
	v_pk_max_f16 v52, v52, 0
	v_pk_max_f16 v50, v50, 0
	v_pk_max_f16 v53, v53, 0
	v_pk_max_f16 v51, v51, 0
	v_pk_fma_f16 v47, v83, v47, v79
	v_pk_fma_f16 v49, v74, v49, v91
	v_pk_fma_f16 v46, v82, v46, v78
	v_pk_fma_f16 v48, v84, v48, v80
	v_pk_max_f16 v44, v44, 0
	v_pk_max_f16 v42, v42, 0
	v_pk_max_f16 v45, v45, 0
	v_pk_max_f16 v43, v43, 0
	v_pk_fma_f16 v39, v83, v39, v76
	v_pk_fma_f16 v41, v74, v41, v81
	v_pk_fma_f16 v40, v84, v40, v77
	v_pk_max_f16 v36, v36, 0
	v_pk_max_f16 v34, v34, 0
	v_pk_max_f16 v37, v37, 0
	v_pk_max_f16 v35, v35, 0
	v_pk_max_f16 v38, v38, 0
	v_pk_max_f16 v64, v64, 0
	v_pk_max_f16 v65, v65, 0
	v_pk_max_f16 v63, v63, 0
	ds_write_b128 v96, v[58:61]
	ds_write_b128 v96, v[62:65] offset:17408
	v_pk_add_f16 v73, v58, v62
	v_pk_max_f16 v56, v56, 0
	v_pk_max_f16 v54, v54, 0
	v_pk_max_f16 v57, v57, 0
	v_pk_max_f16 v55, v55, 0
	ds_write_b128 v96, v[50:53] offset:4352
	ds_write_b128 v96, v[54:57] offset:21760
	v_pk_max_f16 v48, v48, 0
	v_pk_max_f16 v46, v46, 0
	v_pk_max_f16 v49, v49, 0
	v_pk_max_f16 v47, v47, 0
	ds_write_b128 v96, v[42:45] offset:8704
	ds_write_b128 v96, v[46:49] offset:26112
	v_pk_max_f16 v40, v40, 0
	v_pk_max_f16 v41, v41, 0
	v_pk_max_f16 v39, v39, 0
	ds_write_b128 v96, v[34:37] offset:13056
	ds_write_b128 v96, v[38:41] offset:30464
	s_waitcnt lgkmcnt(0)
	s_barrier
	v_pk_add_f16 v62, v34, v38
	v_add_u32_e32 v34, s21, v94
	v_lshl_or_b32 v38, v34, 8, v90
	v_pk_add_f16 v71, v60, v64
	v_pk_add_f16 v60, v35, v39
	v_add_u32_e32 v34, 0x1000, v38
	v_add_u32_e32 v39, 0x2000, v38
	v_pk_add_f16 v69, v61, v65
	v_pk_add_f16 v72, v59, v63
	v_pk_add_f16 v65, v53, v57
	v_pk_add_f16 v67, v52, v56
	v_pk_add_f16 v68, v51, v55
	v_pk_add_f16 v70, v50, v54
	v_pk_add_f16 v61, v45, v49
	v_pk_add_f16 v63, v44, v48
	v_pk_add_f16 v64, v43, v47
	v_pk_add_f16 v66, v42, v46
	v_pk_add_f16 v58, v37, v41
	v_pk_add_f16 v59, v36, v40
	buffer_load_dwordx4 v[100:103], v38, s[8:11], 0 offen sc1
	buffer_load_dwordx4 v[50:53], v34, s[8:11], 0 offen sc1
	v_add_u32_e32 v40, 0x3000, v38
	buffer_load_dwordx4 v[42:45], v39, s[8:11], 0 offen sc1
	buffer_load_dwordx4 v[34:37], v40, s[8:11], 0 offen sc1
	v_add_u32_e32 v39, 0x4000, v38
	v_add_u32_e32 v40, 0x5000, v38
	buffer_load_dwordx4 v[104:107], v39, s[8:11], 0 offen sc1
	buffer_load_dwordx4 v[54:57], v40, s[8:11], 0 offen sc1
	v_add_u32_e32 v90, 0x6000, v38
	v_add_u32_e32 v94, 0x7000, v38
	buffer_load_dwordx4 v[46:49], v90, s[8:11], 0 offen sc1
	buffer_load_dwordx4 v[38:41], v94, s[8:11], 0 offen sc1
	v_mov_b32_e32 v90, v0
	s_waitcnt vmcnt(15)
	v_pk_fma_f16 v27, v83, v27, v88
	v_add_u32_e32 v94, 0xffffff00, v90
	v_lshlrev_b32_e32 v90, 4, v90
	v_ashrrev_i32_e32 v109, 4, v94
	v_and_b32_e32 v108, 0xf0, v90
	v_pk_fma_f16 v29, v74, v29, v95
	v_pk_fma_f16 v26, v82, v26, v87
	v_pk_fma_f16 v28, v84, v28, v92
	s_waitcnt vmcnt(11)
	v_pk_fma_f16 v30, v82, v30, v87
	v_pk_fma_f16 v19, v83, v19, v86
	v_pk_fma_f16 v21, v74, v21, v93
	v_pk_fma_f16 v18, v82, v18, v85
	v_pk_fma_f16 v20, v84, v20, v89
	v_pk_fma_f16 v11, v83, v11, v79
	v_pk_fma_f16 v13, v74, v13, v91
	v_pk_fma_f16 v10, v82, v10, v78
	v_pk_fma_f16 v12, v84, v12, v80
	v_pk_fma_f16 v3, v83, v3, v76
	v_pk_fma_f16 v5, v74, v5, v81
	v_pk_fma_f16 v2, v82, v2, v75
	v_pk_fma_f16 v4, v84, v4, v77
	s_waitcnt vmcnt(8)
	v_pk_fma_f16 v6, v82, v6, v75
	v_pk_fma_f16 v31, v83, v31, v88
	v_pk_fma_f16 v33, v74, v33, v95
	v_pk_fma_f16 v32, v84, v32, v92
	v_pk_max_f16 v28, v28, 0
	v_pk_max_f16 v26, v26, 0
	v_pk_max_f16 v29, v29, 0
	v_pk_max_f16 v27, v27, 0
	v_pk_max_f16 v30, v30, 0
	v_mad_u64_u32 v[110:111], s[24:25], v109, s22, v[108:109]
	v_pk_fma_f16 v23, v83, v23, v86
	v_pk_fma_f16 v25, v74, v25, v93
	v_pk_fma_f16 v22, v82, v22, v85
	v_pk_fma_f16 v24, v84, v24, v89
	v_pk_max_f16 v20, v20, 0
	v_pk_max_f16 v18, v18, 0
	v_pk_max_f16 v21, v21, 0
	v_pk_max_f16 v19, v19, 0
	v_pk_fma_f16 v15, v83, v15, v79
	v_pk_fma_f16 v17, v74, v17, v91
	v_pk_fma_f16 v14, v82, v14, v78
	v_pk_fma_f16 v16, v84, v16, v80
	v_pk_max_f16 v12, v12, 0
	v_pk_max_f16 v10, v10, 0
	v_pk_max_f16 v13, v13, 0
	v_pk_max_f16 v11, v11, 0
	v_pk_fma_f16 v7, v83, v7, v76
	v_pk_fma_f16 v9, v74, v9, v81
	v_pk_fma_f16 v8, v84, v8, v77
	v_pk_max_f16 v4, v4, 0
	v_pk_max_f16 v2, v2, 0
	v_pk_max_f16 v5, v5, 0
	v_pk_max_f16 v3, v3, 0
	v_pk_max_f16 v6, v6, 0
	v_pk_max_f16 v32, v32, 0
	v_pk_max_f16 v33, v33, 0
	v_pk_max_f16 v31, v31, 0
	ds_write_b128 v110, v[26:29] offset:34816
	ds_write_b128 v110, v[30:33] offset:52224
	v_pk_add_f16 v129, v26, v30
	v_pk_max_f16 v24, v24, 0
	v_pk_max_f16 v22, v22, 0
	v_pk_max_f16 v25, v25, 0
	v_pk_max_f16 v23, v23, 0
	ds_write_b128 v110, v[18:21] offset:39168
	ds_write_b128 v110, v[22:25] offset:56576
	v_pk_max_f16 v16, v16, 0
	v_pk_max_f16 v14, v14, 0
	v_pk_max_f16 v17, v17, 0
	v_pk_max_f16 v15, v15, 0
	ds_write_b128 v110, v[10:13] offset:43520
	ds_write_b128 v110, v[14:17] offset:60928
	v_pk_max_f16 v8, v8, 0
	v_pk_max_f16 v9, v9, 0
	v_pk_max_f16 v7, v7, 0
	ds_write_b128 v110, v[2:5] offset:47872
	ds_write_b128 v110, v[6:9] offset:65280
	v_pk_add_f16 v30, v2, v6
	v_add_u32_e32 v2, s19, v109
	v_lshl_or_b32 v6, v2, 8, v108
	v_pk_add_f16 v99, v28, v32
	v_pk_add_f16 v128, v27, v31
	v_pk_add_f16 v27, v4, v8
	v_pk_add_f16 v28, v3, v7
	v_add_u32_e32 v2, 0x1000, v6
	v_add_u32_e32 v7, 0x2000, v6
	v_add_u32_e32 v8, 0x3000, v6
	v_pk_add_f16 v97, v29, v33
	v_pk_add_f16 v33, v21, v25
	v_pk_add_f16 v94, v20, v24
	v_pk_add_f16 v96, v19, v23
	v_pk_add_f16 v98, v18, v22
	v_pk_add_f16 v29, v13, v17
	v_pk_add_f16 v31, v12, v16
	v_pk_add_f16 v32, v11, v15
	v_pk_add_f16 v90, v10, v14
	v_pk_add_f16 v26, v5, v9
	buffer_load_dwordx4 v[108:111], v6, s[8:11], 0 offen sc1
	buffer_load_dwordx4 v[18:21], v2, s[8:11], 0 offen sc1
	buffer_load_dwordx4 v[10:13], v7, s[8:11], 0 offen sc1
	s_nop 0
	buffer_load_dwordx4 v[2:5], v8, s[8:11], 0 offen sc1
	v_add_u32_e32 v7, 0x4000, v6
	v_add_u32_e32 v8, 0x5000, v6
	v_add_u32_e32 v116, 0x6000, v6
	buffer_load_dwordx4 v[112:115], v7, s[8:11], 0 offen sc1
	buffer_load_dwordx4 v[22:25], v8, s[8:11], 0 offen sc1
	v_add_u32_e32 v117, 0x7000, v6
	buffer_load_dwordx4 v[14:17], v116, s[8:11], 0 offen sc1
	buffer_load_dwordx4 v[6:9], v117, s[8:11], 0 offen sc1
	v_fma_mix_f32 v192, v73, s44, 0 op_sel_hi:[1,0,0]
	v_fma_mix_f32 v193, v73, s44, 0 op_sel:[1,0,0] op_sel_hi:[1,0,0]
	v_fma_mix_f32 v192, v129, s44, v192 op_sel_hi:[1,0,0]
	v_fma_mix_f32 v193, v129, s44, v193 op_sel:[1,0,0] op_sel_hi:[1,0,0]
	v_fma_mix_f32 v194, v72, s44, 0 op_sel_hi:[1,0,0]
	v_fma_mix_f32 v195, v72, s44, 0 op_sel:[1,0,0] op_sel_hi:[1,0,0]
	v_fma_mix_f32 v194, v128, s44, v194 op_sel_hi:[1,0,0]
	v_fma_mix_f32 v195, v128, s44, v195 op_sel:[1,0,0] op_sel_hi:[1,0,0]
	v_fma_mix_f32 v196, v71, s44, 0 op_sel_hi:[1,0,0]
	v_fma_mix_f32 v197, v71, s44, 0 op_sel:[1,0,0] op_sel_hi:[1,0,0]
	v_fma_mix_f32 v196, v99, s44, v196 op_sel_hi:[1,0,0]
	v_fma_mix_f32 v197, v99, s44, v197 op_sel:[1,0,0] op_sel_hi:[1,0,0]
	v_fma_mix_f32 v198, v69, s44, 0 op_sel_hi:[1,0,0]
	v_fma_mix_f32 v199, v69, s44, 0 op_sel:[1,0,0] op_sel_hi:[1,0,0]
	v_fma_mix_f32 v198, v97, s44, v198 op_sel_hi:[1,0,0]
	v_fma_mix_f32 v199, v97, s44, v199 op_sel:[1,0,0] op_sel_hi:[1,0,0]
	v_fma_mix_f32 v200, v70, s44, 0 op_sel_hi:[1,0,0]
	v_fma_mix_f32 v201, v70, s44, 0 op_sel:[1,0,0] op_sel_hi:[1,0,0]
	v_fma_mix_f32 v200, v98, s44, v200 op_sel_hi:[1,0,0]
	v_fma_mix_f32 v201, v98, s44, v201 op_sel:[1,0,0] op_sel_hi:[1,0,0]
	v_fma_mix_f32 v202, v68, s44, 0 op_sel_hi:[1,0,0]
	v_fma_mix_f32 v203, v68, s44, 0 op_sel:[1,0,0] op_sel_hi:[1,0,0]
	v_fma_mix_f32 v202, v96, s44, v202 op_sel_hi:[1,0,0]
	v_fma_mix_f32 v203, v96, s44, v203 op_sel:[1,0,0] op_sel_hi:[1,0,0]
	v_fma_mix_f32 v204, v67, s44, 0 op_sel_hi:[1,0,0]
	v_fma_mix_f32 v205, v67, s44, 0 op_sel:[1,0,0] op_sel_hi:[1,0,0]
	v_fma_mix_f32 v204, v94, s44, v204 op_sel_hi:[1,0,0]
	v_fma_mix_f32 v205, v94, s44, v205 op_sel:[1,0,0] op_sel_hi:[1,0,0]
	v_fma_mix_f32 v206, v65, s44, 0 op_sel_hi:[1,0,0]
	v_fma_mix_f32 v207, v65, s44, 0 op_sel:[1,0,0] op_sel_hi:[1,0,0]
	v_fma_mix_f32 v206, v33, s44, v206 op_sel_hi:[1,0,0]
	v_fma_mix_f32 v207, v33, s44, v207 op_sel:[1,0,0] op_sel_hi:[1,0,0]
	v_fma_mix_f32 v208, v66, s44, 0 op_sel_hi:[1,0,0]
	v_fma_mix_f32 v209, v66, s44, 0 op_sel:[1,0,0] op_sel_hi:[1,0,0]
	v_fma_mix_f32 v208, v90, s44, v208 op_sel_hi:[1,0,0]
	v_fma_mix_f32 v209, v90, s44, v209 op_sel:[1,0,0] op_sel_hi:[1,0,0]
	v_fma_mix_f32 v210, v64, s44, 0 op_sel_hi:[1,0,0]
	v_fma_mix_f32 v211, v64, s44, 0 op_sel:[1,0,0] op_sel_hi:[1,0,0]
	v_fma_mix_f32 v210, v32, s44, v210 op_sel_hi:[1,0,0]
	v_fma_mix_f32 v211, v32, s44, v211 op_sel:[1,0,0] op_sel_hi:[1,0,0]
	v_fma_mix_f32 v212, v63, s44, 0 op_sel_hi:[1,0,0]
	v_fma_mix_f32 v213, v63, s44, 0 op_sel:[1,0,0] op_sel_hi:[1,0,0]
	v_fma_mix_f32 v212, v31, s44, v212 op_sel_hi:[1,0,0]
	v_fma_mix_f32 v213, v31, s44, v213 op_sel:[1,0,0] op_sel_hi:[1,0,0]
	v_fma_mix_f32 v214, v61, s44, 0 op_sel_hi:[1,0,0]
	v_fma_mix_f32 v215, v61, s44, 0 op_sel:[1,0,0] op_sel_hi:[1,0,0]
	v_fma_mix_f32 v214, v29, s44, v214 op_sel_hi:[1,0,0]
	v_fma_mix_f32 v215, v29, s44, v215 op_sel:[1,0,0] op_sel_hi:[1,0,0]
	v_fma_mix_f32 v216, v62, s44, 0 op_sel_hi:[1,0,0]
	v_fma_mix_f32 v217, v62, s44, 0 op_sel:[1,0,0] op_sel_hi:[1,0,0]
	v_fma_mix_f32 v216, v30, s44, v216 op_sel_hi:[1,0,0]
	v_fma_mix_f32 v217, v30, s44, v217 op_sel:[1,0,0] op_sel_hi:[1,0,0]
	v_fma_mix_f32 v218, v60, s44, 0 op_sel_hi:[1,0,0]
	v_fma_mix_f32 v219, v60, s44, 0 op_sel:[1,0,0] op_sel_hi:[1,0,0]
	v_fma_mix_f32 v218, v28, s44, v218 op_sel_hi:[1,0,0]
	v_fma_mix_f32 v219, v28, s44, v219 op_sel:[1,0,0] op_sel_hi:[1,0,0]
	v_fma_mix_f32 v220, v59, s44, 0 op_sel_hi:[1,0,0]
	v_fma_mix_f32 v221, v59, s44, 0 op_sel:[1,0,0] op_sel_hi:[1,0,0]
	v_fma_mix_f32 v220, v27, s44, v220 op_sel_hi:[1,0,0]
	v_fma_mix_f32 v221, v27, s44, v221 op_sel:[1,0,0] op_sel_hi:[1,0,0]
	v_fma_mix_f32 v222, v58, s44, 0 op_sel_hi:[1,0,0]
	v_fma_mix_f32 v223, v58, s44, 0 op_sel:[1,0,0] op_sel_hi:[1,0,0]
	v_fma_mix_f32 v222, v26, s44, v222 op_sel_hi:[1,0,0]
	v_fma_mix_f32 v223, v26, s44, v223 op_sel:[1,0,0] op_sel_hi:[1,0,0]
	s_waitcnt lgkmcnt(0)
	s_barrier
	s_lshl_b32 s8, s12, 16
	v_add_u32_e32 v116, 0xffffff00, v130
	v_lshlrev_b32_e32 v117, 3, v130
	v_lshrrev_b32_e32 v131, 4, v116
	v_and_b32_e32 v117, 56, v117
	v_lshrrev_b32_e32 v125, 3, v116
	s_movk_i32 s10, 0xffc0
	s_or_b32 s8, s8, s18
	s_movk_i32 s11, 0x90
	v_or_b32_e32 v120, s8, v117
	ds_read_b128 v[116:119], v162
	v_lshlrev_b32_e32 v133, 1, v120
	ds_read_b128 v[120:123], v162 offset:4608
	s_waitcnt lgkmcnt(1)
	buffer_store_dwordx4 v[116:119], v163, s[4:7], 0 offen sc1
	s_waitcnt vmcnt(16)
	v_pk_fma_f16 v100, v82, v100, v87
	v_add_u32_e32 v116, 0x100, v130
	v_ashrrev_i32_e32 v116, 3, v116
	v_bfi_b32 v135, s10, v116, v125
	ds_read_b128 v[116:119], v162 offset:9216
	ds_read_b128 v[124:127], v162 offset:13824
	s_waitcnt lgkmcnt(2)
	buffer_store_dwordx4 v[120:123], v163, s[4:7], s72 offen sc1
	v_pk_fma_f16 v101, v83, v101, v88
	v_pk_fma_f16 v102, v84, v102, v92
	v_lshl_add_u32 v120, v135, 8, v133
	s_waitcnt lgkmcnt(1)
	buffer_store_dwordx4 v[116:119], v163, s[4:7], s73 offen sc1
	v_pk_fma_f16 v103, v74, v103, v95
	s_waitcnt vmcnt(17)
	v_pk_fma_f16 v50, v82, v50, v85
	s_waitcnt lgkmcnt(0)
	buffer_store_dwordx4 v[124:127], v163, s[4:7], s74 offen sc1
	v_lshlrev_b32_e32 v116, 4, v130
	v_and_b32_e32 v116, 0xf0, v116
	v_pk_fma_f16 v51, v83, v51, v86
	v_pk_fma_f16 v52, v84, v52, v89
	v_pk_fma_f16 v53, v74, v53, v93
	s_waitcnt vmcnt(14)
	v_pk_fma_f16 v56, v84, v56, v89
	v_pk_fma_f16 v57, v74, v57, v93
	v_pk_fma_f16 v42, v82, v42, v78
	v_pk_fma_f16 v43, v83, v43, v79
	v_pk_fma_f16 v44, v84, v44, v80
	v_pk_fma_f16 v45, v74, v45, v91
	s_waitcnt vmcnt(13)
	v_pk_fma_f16 v46, v82, v46, v78
	v_pk_fma_f16 v47, v83, v47, v79
	v_pk_fma_f16 v104, v82, v104, v87
	v_pk_fma_f16 v105, v83, v105, v88
	v_pk_fma_f16 v106, v84, v106, v92
	v_pk_fma_f16 v107, v74, v107, v95
	v_pk_max_f16 v103, v103, 0
	v_pk_max_f16 v102, v102, 0
	v_pk_max_f16 v101, v101, 0
	v_pk_max_f16 v100, v100, 0
	v_mad_u64_u32 v[116:117], s[8:9], v131, s22, v[116:117]
	v_pk_fma_f16 v54, v82, v54, v85
	v_pk_fma_f16 v55, v83, v55, v86
	v_pk_max_f16 v53, v53, 0
	v_pk_max_f16 v52, v52, 0
	v_pk_max_f16 v51, v51, 0
	v_pk_max_f16 v50, v50, 0
	v_pk_max_f16 v57, v57, 0
	v_pk_max_f16 v56, v56, 0
	v_pk_fma_f16 v48, v84, v48, v80
	v_pk_fma_f16 v49, v74, v49, v91
	v_pk_max_f16 v45, v45, 0
	v_pk_max_f16 v44, v44, 0
	v_pk_max_f16 v43, v43, 0
	v_pk_max_f16 v42, v42, 0
	v_pk_max_f16 v47, v47, 0
	v_pk_max_f16 v46, v46, 0
	v_pk_max_f16 v107, v107, 0
	v_pk_max_f16 v106, v106, 0
	v_pk_max_f16 v105, v105, 0
	v_pk_max_f16 v104, v104, 0
	ds_write_b128 v116, v[100:103]
	ds_write_b128 v116, v[104:107] offset:17408
	v_pk_max_f16 v55, v55, 0
	v_pk_max_f16 v54, v54, 0
	ds_write_b128 v116, v[50:53] offset:4352
	ds_write_b128 v116, v[54:57] offset:21760
	v_pk_add_f16 v53, v53, v57
	v_pk_add_f16 v52, v52, v56
	v_pk_max_f16 v49, v49, 0
	v_pk_max_f16 v48, v48, 0
	ds_write_b128 v116, v[42:45] offset:8704
	ds_write_b128 v116, v[46:49] offset:26112
	v_pk_add_f16 v56, v43, v47
	v_pk_add_f16 v57, v42, v46
	v_pk_fma_f16 v34, v82, v34, v75
	v_pk_fma_f16 v35, v83, v35, v76
	v_pk_fma_f16 v36, v84, v36, v77
	v_pk_fma_f16 v37, v74, v37, v81
	s_waitcnt vmcnt(12)
	v_pk_fma_f16 v42, v82, v38, v75
	v_pk_fma_f16 v43, v83, v39, v76
	v_pk_add_f16 v100, v100, v104
	v_pk_add_f16 v51, v51, v55
	v_pk_add_f16 v50, v50, v54
	v_pk_add_f16 v54, v45, v49
	v_pk_add_f16 v55, v44, v48
	v_pk_fma_f16 v44, v84, v40, v77
	v_pk_fma_f16 v45, v74, v41, v81
	v_pk_max_f16 v41, v37, 0
	v_pk_max_f16 v40, v36, 0
	v_pk_max_f16 v39, v35, 0
	v_pk_max_f16 v38, v34, 0
	v_pk_max_f16 v43, v43, 0
	v_pk_max_f16 v42, v42, 0
	v_mov_b32_e32 v104, v0
	v_pk_max_f16 v45, v45, 0
	v_pk_max_f16 v44, v44, 0
	ds_write_b128 v116, v[38:41] offset:13056
	ds_write_b128 v116, v[42:45] offset:30464
	v_pk_add_f16 v36, v39, v43
	v_pk_add_f16 v37, v38, v42
	s_waitcnt lgkmcnt(0)
	s_barrier
	v_pk_add_f16 v101, v101, v105
	v_add_u32_e32 v38, 0xffffff00, v104
	v_lshlrev_b32_e32 v39, 3, v104
	v_lshrrev_b32_e32 v105, 4, v38
	v_and_b32_e32 v39, 56, v39
	v_lshrrev_b32_e32 v47, 3, v38
	v_or_b32_e32 v42, s2, v39
	v_pk_add_f16 v34, v41, v45
	v_pk_add_f16 v35, v40, v44
	ds_read_b128 v[38:41], v162 offset:18432
	v_pk_add_f16 v102, v102, v106
	v_lshlrev_b32_e32 v106, 1, v42
	v_lshrrev_b32_e32 v49, 3, v104
	v_ashrrev_i32_e32 v42, 3, v104
	v_pk_add_f16 v103, v103, v107
	v_bfi_b32 v107, s10, v42, v49
	ds_read_b128 v[42:45], v162 offset:23040
	s_waitcnt lgkmcnt(1)
	buffer_store_dwordx4 v[38:41], v163, s[4:7], s75 offen sc1
	v_lshl_add_u32 v107, v107, 8, v106
	s_waitcnt vmcnt(11)
	v_pk_fma_f16 v18, v82, v18, v85
	v_add_u32_e32 v38, 0x100, v104
	v_ashrrev_i32_e32 v38, 3, v38
	v_bfi_b32 v116, s10, v38, v47
	v_add_u32_e32 v47, 0x200, v104
	v_ashrrev_i32_e32 v47, 3, v47
	v_bfi_b32 v117, s10, v47, v49
	ds_read_b128 v[38:41], v162 offset:27648
	ds_read_b128 v[46:49], v162 offset:32256
	s_waitcnt lgkmcnt(2)
	buffer_store_dwordx4 v[42:45], v163, s[4:7], s76 offen sc1
	v_pk_fma_f16 v19, v83, v19, v86
	v_pk_fma_f16 v20, v84, v20, v89
	s_waitcnt lgkmcnt(1)
	buffer_store_dwordx4 v[38:41], v163, s[4:7], s77 offen sc1
	v_pk_fma_f16 v21, v74, v21, v93
	s_waitcnt vmcnt(9)
	v_pk_fma_f16 v24, v84, v24, v89
	s_waitcnt lgkmcnt(0)
	buffer_store_dwordx4 v[46:49], v163, s[4:7], s78 offen sc1
	v_lshlrev_b32_e32 v38, 4, v104
	v_pk_fma_f16 v39, v83, v109, v88
	v_and_b32_e32 v46, 0xf0, v38
	v_pk_fma_f16 v38, v82, v108, v87
	v_pk_fma_f16 v40, v84, v110, v92
	v_pk_fma_f16 v41, v74, v111, v95
	v_pk_fma_f16 v25, v74, v25, v93
	v_pk_fma_f16 v10, v82, v10, v78
	v_pk_fma_f16 v11, v83, v11, v79
	v_pk_fma_f16 v12, v84, v12, v80
	v_pk_fma_f16 v13, v74, v13, v91
	v_pk_fma_f16 v2, v82, v2, v75
	v_pk_fma_f16 v3, v83, v3, v76
	v_pk_fma_f16 v4, v84, v4, v77
	v_pk_fma_f16 v5, v74, v5, v81
	s_waitcnt vmcnt(8)
	v_pk_fma_f16 v6, v82, v6, v75
	v_pk_fma_f16 v7, v83, v7, v76
	v_pk_fma_f16 v42, v82, v112, v87
	v_pk_fma_f16 v43, v83, v113, v88
	v_pk_fma_f16 v44, v84, v114, v92
	v_pk_fma_f16 v45, v74, v115, v95
	v_pk_max_f16 v41, v41, 0
	v_pk_max_f16 v40, v40, 0
	v_pk_max_f16 v39, v39, 0
	v_pk_max_f16 v38, v38, 0
	v_mad_u64_u32 v[46:47], s[8:9], v105, s22, v[46:47]
	v_pk_fma_f16 v22, v82, v22, v85
	v_pk_fma_f16 v23, v83, v23, v86
	v_pk_max_f16 v21, v21, 0
	v_pk_max_f16 v20, v20, 0
	v_pk_max_f16 v19, v19, 0
	v_pk_max_f16 v18, v18, 0
	v_pk_max_f16 v25, v25, 0
	v_pk_max_f16 v24, v24, 0
	v_pk_fma_f16 v14, v82, v14, v78
	v_pk_fma_f16 v15, v83, v15, v79
	v_pk_fma_f16 v16, v84, v16, v80
	v_pk_fma_f16 v17, v74, v17, v91
	v_pk_max_f16 v13, v13, 0
	v_pk_max_f16 v12, v12, 0
	v_pk_max_f16 v11, v11, 0
	v_pk_max_f16 v10, v10, 0
	v_pk_fma_f16 v8, v84, v8, v77
	v_pk_fma_f16 v9, v74, v9, v81
	v_pk_max_f16 v5, v5, 0
	v_pk_max_f16 v4, v4, 0
	v_pk_max_f16 v3, v3, 0
	v_pk_max_f16 v2, v2, 0
	v_pk_max_f16 v7, v7, 0
	v_pk_max_f16 v6, v6, 0
	v_pk_max_f16 v45, v45, 0
	v_pk_max_f16 v44, v44, 0
	v_pk_max_f16 v43, v43, 0
	v_pk_max_f16 v42, v42, 0
	ds_write_b128 v46, v[38:41] offset:34816
	ds_write_b128 v46, v[42:45] offset:52224
	v_pk_max_f16 v23, v23, 0
	v_pk_max_f16 v22, v22, 0
	ds_write_b128 v46, v[18:21] offset:39168
	ds_write_b128 v46, v[22:25] offset:56576
	v_pk_add_f16 v21, v21, v25
	v_pk_add_f16 v20, v20, v24
	v_pk_max_f16 v17, v17, 0
	v_pk_max_f16 v16, v16, 0
	v_pk_max_f16 v15, v15, 0
	v_pk_max_f16 v14, v14, 0
	ds_write_b128 v46, v[10:13] offset:43520
	ds_write_b128 v46, v[14:17] offset:60928
	v_pk_max_f16 v9, v9, 0
	v_pk_max_f16 v8, v8, 0
	ds_write_b128 v46, v[2:5] offset:47872
	ds_write_b128 v46, v[6:9] offset:65280
	v_pk_add_f16 v24, v3, v7
	v_pk_add_f16 v25, v2, v6
	v_pk_add_f16 v19, v19, v23
	v_pk_add_f16 v18, v18, v22
	v_pk_add_f16 v22, v5, v9
	v_pk_add_f16 v23, v4, v8
	v_pk_add_f16 v38, v38, v42
	v_fma_mix_f32 v192, v100, s44, v192 op_sel_hi:[1,0,0]
	v_fma_mix_f32 v193, v100, s44, v193 op_sel:[1,0,0] op_sel_hi:[1,0,0]
	v_fma_mixlo_f16 v224, v38, s44, v192 op_sel_hi:[1,0,0]
	s_nop 0
	v_fma_mixhi_f16 v224, v38, s44, v193 op_sel:[1,0,0] op_sel_hi:[1,0,0]
	v_pk_add_f16 v39, v39, v43
	v_fma_mix_f32 v194, v101, s44, v194 op_sel_hi:[1,0,0]
	v_fma_mix_f32 v195, v101, s44, v195 op_sel:[1,0,0] op_sel_hi:[1,0,0]
	v_pk_add_f16 v15, v11, v15
	v_pk_add_f16 v14, v10, v14
	v_fma_mixlo_f16 v225, v39, s44, v194 op_sel_hi:[1,0,0]
	s_nop 0
	v_fma_mixhi_f16 v225, v39, s44, v195 op_sel:[1,0,0] op_sel_hi:[1,0,0]
	s_mov_b32 s2, 0x3e000000
	v_pk_add_f16 v40, v40, v44
	v_fma_mix_f32 v196, v102, s44, v196 op_sel_hi:[1,0,0]
	v_fma_mix_f32 v197, v102, s44, v197 op_sel:[1,0,0] op_sel_hi:[1,0,0]
	v_fma_mixlo_f16 v226, v40, s44, v196 op_sel_hi:[1,0,0]
	s_nop 0
	v_fma_mixhi_f16 v226, v40, s44, v197 op_sel:[1,0,0] op_sel_hi:[1,0,0]
	v_pk_add_f16 v41, v41, v45
	v_fma_mix_f32 v198, v103, s44, v198 op_sel_hi:[1,0,0]
	v_fma_mix_f32 v199, v103, s44, v199 op_sel:[1,0,0] op_sel_hi:[1,0,0]
	v_pk_add_f16 v17, v13, v17
	v_pk_add_f16 v16, v12, v16
	v_fma_mixlo_f16 v227, v41, s44, v198 op_sel_hi:[1,0,0]
	s_nop 0
	v_fma_mixhi_f16 v227, v41, s44, v199 op_sel:[1,0,0] op_sel_hi:[1,0,0]
	v_add_u32_e32 v38, 0x1a000, v46
	v_fma_mix_f32 v200, v18, s44, v200 op_sel_hi:[1,0,0]
	v_fma_mix_f32 v201, v18, s44, v201 op_sel:[1,0,0] op_sel_hi:[1,0,0]
	ds_write_b128 v38, v[224:227]
	v_fma_mixlo_f16 v228, v50, s44, v200 op_sel_hi:[1,0,0]
	s_nop 0
	v_fma_mixhi_f16 v228, v50, s44, v201 op_sel:[1,0,0] op_sel_hi:[1,0,0]
	v_fma_mix_f32 v202, v19, s44, v202 op_sel_hi:[1,0,0]
	s_nop 0
	v_fma_mixlo_f16 v229, v51, s44, v202 op_sel_hi:[1,0,0]
	v_fma_mix_f32 v203, v51, s44, v203 op_sel:[1,0,0] op_sel_hi:[1,0,0]
	v_fma_mixhi_f16 v229, v19, s44, v203 op_sel:[1,0,0] op_sel_hi:[1,0,0]
	v_fma_mix_f32 v204, v52, s44, v204 op_sel_hi:[1,0,0]
	v_fma_mix_f32 v205, v52, s44, v205 op_sel:[1,0,0] op_sel_hi:[1,0,0]
	v_fma_mixlo_f16 v230, v20, s44, v204 op_sel_hi:[1,0,0]
	s_nop 0
	v_fma_mixhi_f16 v230, v20, s44, v205 op_sel:[1,0,0] op_sel_hi:[1,0,0]
	v_fma_mix_f32 v206, v21, s44, v206 op_sel_hi:[1,0,0]
	s_nop 0
	v_fma_mixlo_f16 v231, v53, s44, v206 op_sel_hi:[1,0,0]
	v_fma_mix_f32 v207, v53, s44, v207 op_sel:[1,0,0] op_sel_hi:[1,0,0]
	v_fma_mixhi_f16 v231, v21, s44, v207 op_sel:[1,0,0] op_sel_hi:[1,0,0]
	v_fma_mix_f32 v208, v14, s44, v208 op_sel_hi:[1,0,0]
	v_fma_mix_f32 v209, v14, s44, v209 op_sel:[1,0,0] op_sel_hi:[1,0,0]
	v_fma_mix_f32 v210, v15, s44, v210 op_sel_hi:[1,0,0]
	ds_write_b128 v38, v[228:231] offset:4352
	v_fma_mixlo_f16 v232, v57, s44, v208 op_sel_hi:[1,0,0]
	s_nop 0
	v_fma_mixhi_f16 v232, v57, s44, v209 op_sel:[1,0,0] op_sel_hi:[1,0,0]
	v_fma_mix_f32 v211, v15, s44, v211 op_sel:[1,0,0] op_sel_hi:[1,0,0]
	v_fma_mixlo_f16 v233, v56, s44, v210 op_sel_hi:[1,0,0]
	s_nop 0
	v_fma_mixhi_f16 v233, v56, s44, v211 op_sel:[1,0,0] op_sel_hi:[1,0,0]
	v_fma_mix_f32 v212, v55, s44, v212 op_sel_hi:[1,0,0]
	v_fma_mix_f32 v213, v55, s44, v213 op_sel:[1,0,0] op_sel_hi:[1,0,0]
	v_fma_mixlo_f16 v234, v16, s44, v212 op_sel_hi:[1,0,0]
	s_nop 0
	v_fma_mixhi_f16 v234, v16, s44, v213 op_sel:[1,0,0] op_sel_hi:[1,0,0]
	v_fma_mix_f32 v214, v17, s44, v214 op_sel_hi:[1,0,0]
	s_nop 0
	v_fma_mixlo_f16 v235, v54, s44, v214 op_sel_hi:[1,0,0]
	v_fma_mix_f32 v215, v54, s44, v215 op_sel:[1,0,0] op_sel_hi:[1,0,0]
	v_fma_mixhi_f16 v235, v17, s44, v215 op_sel:[1,0,0] op_sel_hi:[1,0,0]
	v_fma_mix_f32 v216, v25, s44, v216 op_sel_hi:[1,0,0]
	v_fma_mix_f32 v217, v25, s44, v217 op_sel:[1,0,0] op_sel_hi:[1,0,0]
	v_fma_mix_f32 v218, v24, s44, v218 op_sel_hi:[1,0,0]
	ds_write_b128 v38, v[232:235] offset:8704
	v_fma_mixlo_f16 v236, v37, s44, v216 op_sel_hi:[1,0,0]
	s_nop 0
	v_fma_mixhi_f16 v236, v37, s44, v217 op_sel:[1,0,0] op_sel_hi:[1,0,0]
	v_fma_mix_f32 v219, v24, s44, v219 op_sel:[1,0,0] op_sel_hi:[1,0,0]
	v_fma_mixlo_f16 v237, v36, s44, v218 op_sel_hi:[1,0,0]
	s_nop 0
	v_fma_mixhi_f16 v237, v36, s44, v219 op_sel:[1,0,0] op_sel_hi:[1,0,0]
	v_fma_mix_f32 v220, v35, s44, v220 op_sel_hi:[1,0,0]
	v_fma_mix_f32 v221, v35, s44, v221 op_sel:[1,0,0] op_sel_hi:[1,0,0]
	v_fma_mixlo_f16 v238, v23, s44, v220 op_sel_hi:[1,0,0]
	s_nop 0
	v_fma_mixhi_f16 v238, v23, s44, v221 op_sel:[1,0,0] op_sel_hi:[1,0,0]
	v_fma_mix_f32 v222, v22, s44, v222 op_sel_hi:[1,0,0]
	s_nop 0
	v_fma_mixlo_f16 v239, v34, s44, v222 op_sel_hi:[1,0,0]
	v_fma_mix_f32 v223, v34, s44, v223 op_sel:[1,0,0] op_sel_hi:[1,0,0]
	v_fma_mixhi_f16 v239, v22, s44, v223 op_sel:[1,0,0] op_sel_hi:[1,0,0]
	s_cmpk_lt_u32 s15, 0x180
	s_cselect_b64 s[8:9], -1, 0
	s_cmpk_gt_u32 s15, 0x17f
	ds_write_b128 v38, v[236:239] offset:13056
	s_cbranch_scc1 .LBB3_3
	s_load_dwordx2 s[10:11], s[0:1], 0x78
	s_load_dwordx4 s[24:27], s[0:1], 0x50
	v_mov_b32_e32 v2, v0
	s_lshl_b64 s[22:23], s[12:13], 12
	s_waitcnt lgkmcnt(0)
	s_add_u32 s10, s10, s22
	v_lshlrev_b32_e32 v2, 3, v2
	s_addc_u32 s11, s11, s23
	v_and_b32_e32 v2, 0x1f8, v2
	global_load_dwordx2 v[136:137], v2, s[10:11]
	global_load_dwordx2 v[132:133], v2, s[10:11] offset:512
	global_load_dwordx2 v[128:129], v2, s[10:11] offset:1024
	global_load_dwordx2 v[124:125], v2, s[10:11] offset:1536
	global_load_dwordx2 v[134:135], v2, s[10:11] offset:2048
	global_load_dwordx2 v[130:131], v2, s[10:11] offset:2560
	global_load_dwordx2 v[126:127], v2, s[10:11] offset:3072
	global_load_dwordx2 v[122:123], v2, s[10:11] offset:3584
	s_lshl_b32 s2, s14, 4
	s_lshl_b32 s10, s17, 3
	s_add_i32 s10, s10, s2
	s_sub_i32 s2, s10, 32
	s_lshl_b64 s[2:3], s[2:3], 10
	v_lshl_or_b32 v2, v2, 1, s2
	v_mov_b32_e32 v3, s3
	v_lshl_add_u64 v[4:5], s[24:25], 0, v[2:3]
	global_load_dwordx4 v[18:21], v[4:5], off
	global_load_dwordx4 v[102:105], v[4:5], off offset:1024
	global_load_dwordx4 v[94:97], v[4:5], off offset:2048
	global_load_dwordx4 v[86:89], v[4:5], off offset:3072
	v_add_co_u32_e32 v4, vcc, s20, v4
	v_lshl_add_u64 v[6:7], s[26:27], 0, v[2:3]
	s_nop 0
	v_addc_co_u32_e32 v5, vcc, 0, v5, vcc
	global_load_dwordx4 v[78:81], v[4:5], off
	global_load_dwordx4 v[74:77], v[4:5], off offset:1024
	global_load_dwordx4 v[70:73], v[4:5], off offset:2048
	global_load_dwordx4 v[66:69], v[4:5], off offset:3072
	s_nop 0
	global_load_dwordx4 v[2:5], v[6:7], off
	global_load_dwordx4 v[118:121], v[6:7], off offset:1024
	global_load_dwordx4 v[114:117], v[6:7], off offset:2048
	global_load_dwordx4 v[110:113], v[6:7], off offset:3072
	v_add_co_u32_e32 v6, vcc, s20, v6
	s_nop 1
	v_addc_co_u32_e32 v7, vcc, 0, v7, vcc
	global_load_dwordx4 v[106:109], v[6:7], off
	global_load_dwordx4 v[98:101], v[6:7], off offset:1024
	global_load_dwordx4 v[90:93], v[6:7], off offset:2048
	global_load_dwordx4 v[82:85], v[6:7], off offset:3072
	s_branch .LBB3_4

.LBB3_10:
	v_mov_b32_e32 v11, v0
	s_waitcnt lgkmcnt(0)
	s_barrier
	s_lshl_b32 s8, s19, 7
	s_waitcnt vmcnt(7)
	ds_read_b128 v[2:5], v162 offset:18432
	ds_read_b128 v[6:9], v162 offset:23040
	ds_read_b128 v[10:13], v162 offset:27648
	ds_read_b128 v[14:17], v162 offset:32256
	s_waitcnt lgkmcnt(3)
	buffer_store_dwordx4 v[2:5], v163, s[4:7], s66 offen sc1
	s_waitcnt lgkmcnt(2)
	buffer_store_dwordx4 v[6:9], v163, s[4:7], s67 offen sc1
	s_waitcnt lgkmcnt(1)
	buffer_store_dwordx4 v[10:13], v163, s[4:7], s68 offen sc1
	s_waitcnt lgkmcnt(0)
	buffer_store_dwordx4 v[14:17], v163, s[4:7], s69 offen sc1
	s_movk_i32 s4, 0x13f
	v_cmp_lt_u32_e32 vcc, s4, v0
	s_and_saveexec_b64 s[4:5], vcc
	s_xor_b64 s[4:5], exec, s[4:5]
	s_cbranch_execz .LBB3_14
	s_movk_i32 s6, 0x180
	v_cmp_gt_u32_e32 vcc, s6, v0
	s_and_saveexec_b64 s[6:7], vcc
	s_cbranch_execz .LBB3_13
	v_mov_b32_e32 v2, 0x1e400
	v_lshl_add_u32 v1, v1, 2, v2
	s_lshl_b32 s8, s16, 8
	ds_read_b32 v1, v1
	s_or_b32 s8, s18, s8
	v_add_u32_e32 v2, s8, v0
	v_add_u32_e32 v2, 0xffffff40, v2
	v_mov_b32_e32 v3, 0
	v_lshl_add_u64 v[2:3], v[2:3], 2, s[2:3]
	s_waitcnt lgkmcnt(0)
	global_atomic_add_f32 v[2:3], v1, off

amdhsa.kernels:
  - .agpr_count:     32
    .args:
      - .actual_access:  read_only
        .address_space:  global
        .offset:         0
        .size:           8
        .value_kind:     global_buffer
      - .actual_access:  read_only
        .address_space:  global
        .offset:         8
        .size:           8
        .value_kind:     global_buffer
      - .actual_access:  read_only
        .address_space:  global
        .offset:         16
        .size:           8
        .value_kind:     global_buffer
      - .actual_access:  write_only
        .address_space:  global
        .offset:         24
        .size:           8
        .value_kind:     global_buffer
      - .actual_access:  read_only
        .address_space:  global
        .offset:         32
        .size:           8
        .value_kind:     global_buffer
      - .actual_access:  read_only
        .address_space:  global
        .offset:         40
        .size:           8
        .value_kind:     global_buffer
      - .actual_access:  read_only
        .address_space:  global
        .offset:         48
        .size:           8
        .value_kind:     global_buffer
      - .actual_access:  read_only
        .address_space:  global
        .offset:         56
        .size:           8
        .value_kind:     global_buffer
      - .actual_access:  read_only
        .address_space:  global
        .offset:         64
        .size:           8
        .value_kind:     global_buffer
      - .actual_access:  read_only
        .address_space:  global
        .offset:         72
        .size:           8
        .value_kind:     global_buffer
      - .actual_access:  read_only
        .address_space:  global
        .offset:         80
        .size:           8
        .value_kind:     global_buffer
      - .actual_access:  write_only
        .address_space:  global
        .offset:         88
        .size:           8
        .value_kind:     global_buffer
      - .actual_access:  write_only
        .address_space:  global
        .offset:         96
        .size:           8
        .value_kind:     global_buffer
      - .actual_access:  write_only
        .address_space:  global
        .offset:         104
        .size:           8
        .value_kind:     global_buffer
      - .actual_access:  write_only
        .address_space:  global
        .offset:         112
        .size:           8
        .value_kind:     global_buffer
      - .actual_access:  write_only
        .address_space:  global
        .offset:         120
        .size:           8
        .value_kind:     global_buffer
    .group_segment_fixed_size: 17408
    .kernarg_segment_align: 8
    .kernarg_segment_size: 128
    .language:       OpenCL C
    .language_version:
      - 2
      - 0
    .max_flat_workgroup_size: 256
    .name:           _Z9k_encprepPKfS0_S0_PDF16_PKiS3_S0_S0_S0_S0_S0_PhS4_S1_S1_Pf
    .private_segment_fixed_size: 0
    .sgpr_count:     22
    .sgpr_spill_count: 0
    .symbol:         _Z9k_encprepPKfS0_S0_PDF16_PKiS3_S0_S0_S0_S0_S0_PhS4_S1_S1_Pf.kd
    .uniform_work_group_size: 1
    .uses_dynamic_stack: false
    .vgpr_count:     128
    .vgpr_spill_count: 0
    .wavefront_size: 64
  - .agpr_count:     0
    .args:
      - .actual_access:  read_only
        .address_space:  global
        .offset:         0
        .size:           8
        .value_kind:     global_buffer
      - .actual_access:  read_only
        .address_space:  global
        .offset:         8
        .size:           8
        .value_kind:     global_buffer
      - .actual_access:  read_only
        .address_space:  global
        .offset:         16
        .size:           8
        .value_kind:     global_buffer
      - .actual_access:  read_only
        .address_space:  global
        .offset:         24
        .size:           8
        .value_kind:     global_buffer
      - .actual_access:  read_only
        .address_space:  global
        .offset:         32
        .size:           8
        .value_kind:     global_buffer
      - .actual_access:  read_only
        .address_space:  global
        .offset:         40
        .size:           8
        .value_kind:     global_buffer
      - .actual_access:  read_only
        .address_space:  global
        .offset:         48
        .size:           8
        .value_kind:     global_buffer
      - .actual_access:  read_only
        .address_space:  global
        .offset:         56
        .size:           8
        .value_kind:     global_buffer
      - .actual_access:  read_only
        .address_space:  global
        .offset:         64
        .size:           8
        .value_kind:     global_buffer
      - .actual_access:  read_only
        .address_space:  global
        .offset:         72
        .size:           8
        .value_kind:     global_buffer
      - .actual_access:  read_only
        .address_space:  global
        .offset:         80
        .size:           8
        .value_kind:     global_buffer
      - .actual_access:  read_only
        .address_space:  global
        .offset:         88
        .size:           8
        .value_kind:     global_buffer
      - .actual_access:  write_only
        .address_space:  global
        .offset:         96
        .size:           8
        .value_kind:     global_buffer
    .group_segment_fixed_size: 40448
    .kernarg_segment_align: 8
    .kernarg_segment_size: 104
    .language:       OpenCL C
    .language_version:
      - 2
      - 0
    .max_flat_workgroup_size: 1024
    .name:           _Z7k_finalPKDF16_S0_PKfS2_S2_S2_S2_S2_S0_S2_S2_S2_Pf
    .private_segment_fixed_size: 0
    .sgpr_count:     24
    .sgpr_spill_count: 0
    .symbol:         _Z7k_finalPKDF16_S0_PKfS2_S2_S2_S2_S2_S0_S2_S2_S2_Pf.kd
    .uniform_work_group_size: 1
    .uses_dynamic_stack: false
    .vgpr_count:     99
    .vgpr_spill_count: 0
    .wavefront_size: 64
  - .agpr_count:     0
    .args:
      - .actual_access:  read_only
        .address_space:  global
        .offset:         0
        .size:           8
        .value_kind:     global_buffer
      - .actual_access:  read_only
        .address_space:  global
        .offset:         8
        .size:           8
        .value_kind:     global_buffer
      - .actual_access:  read_only
        .address_space:  global
        .offset:         16
        .size:           8
        .value_kind:     global_buffer
      - .actual_access:  read_only
        .address_space:  global
        .offset:         24
        .size:           8
        .value_kind:     global_buffer
      - .actual_access:  read_only
        .address_space:  global
        .offset:         32
        .size:           8
        .value_kind:     global_buffer
      - .actual_access:  read_only
        .address_space:  global
        .offset:         40
        .size:           8
        .value_kind:     global_buffer
      - .actual_access:  read_only
        .address_space:  global
        .offset:         48
        .size:           8
        .value_kind:     global_buffer
      - .actual_access:  read_only
        .address_space:  global
        .offset:         56
        .size:           8
        .value_kind:     global_buffer
      - .actual_access:  read_only
        .address_space:  global
        .offset:         64
        .size:           8
        .value_kind:     global_buffer
      - .actual_access:  read_only
        .address_space:  global
        .offset:         72
        .size:           8
        .value_kind:     global_buffer
      - .actual_access:  read_only
        .address_space:  global
        .offset:         80
        .size:           8
        .value_kind:     global_buffer
      - .actual_access:  read_only
        .address_space:  global
        .offset:         88
        .size:           8
        .value_kind:     global_buffer
      - .actual_access:  read_only
        .address_space:  global
        .offset:         96
        .size:           8
        .value_kind:     global_buffer
      - .actual_access:  read_only
        .address_space:  global
        .offset:         104
        .size:           8
        .value_kind:     global_buffer
      - .actual_access:  read_only
        .address_space:  global
        .offset:         112
        .size:           8
        .value_kind:     global_buffer
      - .actual_access:  read_only
        .address_space:  global
        .offset:         120
        .size:           8
        .value_kind:     global_buffer
      - .actual_access:  write_only
        .address_space:  global
        .offset:         128
        .size:           8
        .value_kind:     global_buffer
      - .actual_access:  write_only
        .address_space:  global
        .offset:         136
        .size:           8
        .value_kind:     global_buffer
      - .address_space:  global
        .offset:         144
        .size:           8
        .value_kind:     global_buffer
      - .address_space:  global
        .offset:         152
        .size:           8
        .value_kind:     global_buffer
    .group_segment_fixed_size: 126720
    .kernarg_segment_align: 8
    .kernarg_segment_size: 160
    .language:       OpenCL C
    .language_version:
      - 2
      - 0
    .max_flat_workgroup_size: 512
    .name:           _Z7k_layerILi1EEvPKDF16_S1_PKfS3_S3_S3_S3_S3_S1_S1_S1_S1_S3_S3_PKhS5_PDF16_S6_PfS7_
    .private_segment_fixed_size: 0
    .sgpr_count:     80
    .sgpr_spill_count: 0
    .symbol:         _Z7k_layerILi1EEvPKDF16_S1_PKfS3_S3_S3_S3_S3_S1_S1_S1_S1_S3_S3_PKhS5_PDF16_S6_PfS7_.kd
    .uniform_work_group_size: 1
    .uses_dynamic_stack: false
    .vgpr_count:     256
    .vgpr_spill_count: 0
    .wavefront_size: 64
  - .agpr_count:     0
    .args:
      - .actual_access:  read_only
        .address_space:  global
        .offset:         0
        .size:           8
        .value_kind:     global_buffer
      - .actual_access:  read_only
        .address_space:  global
        .offset:         8
        .size:           8
        .value_kind:     global_buffer
      - .actual_access:  read_only
        .address_space:  global
        .offset:         16
        .size:           8
        .value_kind:     global_buffer
      - .actual_access:  read_only
        .address_space:  global
        .offset:         24
        .size:           8
        .value_kind:     global_buffer
      - .actual_access:  read_only
        .address_space:  global
        .offset:         32
        .size:           8
        .value_kind:     global_buffer
      - .actual_access:  read_only
        .address_space:  global
        .offset:         40
        .size:           8
        .value_kind:     global_buffer
      - .actual_access:  read_only
        .address_space:  global
        .offset:         48
        .size:           8
        .value_kind:     global_buffer
      - .actual_access:  read_only
        .address_space:  global
        .offset:         56
        .size:           8
        .value_kind:     global_buffer
      - .actual_access:  read_only
        .address_space:  global
        .offset:         64
        .size:           8
        .value_kind:     global_buffer
      - .actual_access:  read_only
        .address_space:  global
        .offset:         72
        .size:           8
        .value_kind:     global_buffer
      - .actual_access:  read_only
        .address_space:  global
        .offset:         80
        .size:           8
        .value_kind:     global_buffer
      - .actual_access:  read_only
        .address_space:  global
        .offset:         88
        .size:           8
        .value_kind:     global_buffer
      - .actual_access:  read_only
        .address_space:  global
        .offset:         96
        .size:           8
        .value_kind:     global_buffer
      - .actual_access:  read_only
        .address_space:  global
        .offset:         104
        .size:           8
        .value_kind:     global_buffer
      - .actual_access:  read_only
        .address_space:  global
        .offset:         112
        .size:           8
        .value_kind:     global_buffer
      - .actual_access:  read_only
        .address_space:  global
        .offset:         120
        .size:           8
        .value_kind:     global_buffer
      - .actual_access:  write_only
        .address_space:  global
        .offset:         128
        .size:           8
        .value_kind:     global_buffer
      - .actual_access:  write_only
        .address_space:  global
        .offset:         136
        .size:           8
        .value_kind:     global_buffer
      - .address_space:  global
        .offset:         144
        .size:           8
        .value_kind:     global_buffer
      - .address_space:  global
        .offset:         152
        .size:           8
        .value_kind:     global_buffer
    .group_segment_fixed_size: 126720
    .kernarg_segment_align: 8
    .kernarg_segment_size: 160
    .language:       OpenCL C
    .language_version:
      - 2
      - 0
    .max_flat_workgroup_size: 512
    .name:           _Z7k_layerILi0EEvPKDF16_S1_PKfS3_S3_S3_S3_S3_S1_S1_S1_S1_S3_S3_PKhS5_PDF16_S6_PfS7_
    .private_segment_fixed_size: 0
    .sgpr_count:     80
    .sgpr_spill_count: 0
    .symbol:         _Z7k_layerILi0EEvPKDF16_S1_PKfS3_S3_S3_S3_S3_S1_S1_S1_S1_S3_S3_PKhS5_PDF16_S6_PfS7_.kd
    .uniform_work_group_size: 1
    .uses_dynamic_stack: false
    .vgpr_count:     256
    .vgpr_spill_count: 0
    .wavefront_size: 64
